# counted vmcnt waits in 5 expert-weight conversion loops (double buffering restored)
# speedup vs baseline: 1.0115x; 1.0115x over previous
; #define LAS __attribute__((address_space(3)))
; __device__ __forceinline__ unsigned pk2(float lo, float hi) { return f2bf(lo) | (f2bf(hi) << 16); }
;     __device__ __forceinline__ const float* x() const { return (const float*)ld(0); }
;     __device__ __forceinline__ const float* c() const { return (const float*)ld(1); }
; template <bool NT = true> __device__ __forceinline__ void cvt_store(const CvtItem& d, const f32x4 (&v)[8], LAS float* scr, int lane) {
;     const int rr = lane >> 3, c4 = (lane & 7) * 4;
; #pragma unroll
;     for (int q = 0; q < 8; ++q) { LAS float* t = scr + (8 * q + rr) * 33 + c4; t[0] = v[q].x; t[1] = v[q].y; t[2] = v[q].z; t[3] = v[q].w; }
;     asm volatile("s_waitcnt lgkmcnt(0)" ::: "memory");
;     const int c = lane & 7;
; #pragma unroll
;     for (int j = 0; j < 4; ++j) { const int n = (lane >> 3) + 8 * j; const LAS float* s = scr + (8 * c) * 33 + n;
;         u32x4 o; o.x = pk2(s[0 * 33], s[1 * 33]); o.y = pk2(s[2 * 33], s[3 * 33]); o.z = pk2(s[4 * 33], s[5 * 33]); o.w = pk2(s[6 * 33], s[7 * 33]);
;         const int ng = d.n0 + n, drow = d.row_off + (d.ilv ? ((ng >> 7) * 256 + (ng & 127)) : ng);
;         if (NT) __builtin_nontemporal_store(o, (u32x4*)(d.dst + (size_t)drow * d.K + d.k0 + 8 * c)); else *(u32x4*)(d.dst + (size_t)drow * d.K + d.k0 + 8 * c) = o; }
;     asm volatile("s_waitcnt lgkmcnt(0)" ::: "memory");
; }
; __device__ __forceinline__ void convert_moe_items(const Ctx& a, int layer, LAS unsigned char* lds, int it0, int it1, int widx, int nw, int wave, int lane) {
;     ...
;     for (;;) {
;         cvt_store(da, va, scr, lane);
;         it += 2 * nw; const bool ha = (it < it1);
;         if (ha) { da = decode(it); cvt_load(da, va, lane); }
.LBB0_148:
	s_cmp_lg_u64 s[16:17], 0
	s_cbranch_scc1 .Lcvt_p0m_t
	s_waitcnt vmcnt(0)
.Lcvt_p0m_t:
	v_add_u32_e32 v79, 0x420, v74
	v_add_u32_e32 v80, 0x428, v74
	v_add_u32_e32 v81, 0x840, v74
	v_add_u32_e32 v82, 0x848, v74
	v_add_u32_e32 v83, 0xc60, v74
	v_add_u32_e32 v84, 0xc68, v74
	v_add_u32_e32 v85, 0x1080, v74
	v_add_u32_e32 v86, 0x1088, v74
	v_add_u32_e32 v87, 0x14a0, v74
	v_add_u32_e32 v88, 0x14a8, v74
	v_add_u32_e32 v89, 0x18c0, v74
	v_add_u32_e32 v90, 0x18c8, v74
	v_add_u32_e32 v91, 0x1ce0, v74
	v_add_u32_e32 v92, 0x1ce8, v74
	s_waitcnt vmcnt(15)
	ds_write2_b32 v74, v2, v3 offset1:1
	ds_write2_b32 v74, v4, v5 offset0:2 offset1:3
	s_waitcnt vmcnt(14)
	ds_write2_b32 v79, v6, v7 offset1:1
	ds_write2_b32 v80, v8, v9 offset1:1
	s_waitcnt vmcnt(13)
	ds_write2_b32 v81, v10, v11 offset1:1
	ds_write2_b32 v82, v12, v13 offset1:1
	s_waitcnt vmcnt(12)
	ds_write2_b32 v83, v14, v15 offset1:1
	ds_write2_b32 v84, v16, v17 offset1:1
	s_waitcnt vmcnt(11)
	ds_write2_b32 v85, v18, v19 offset1:1
	ds_write2_b32 v86, v20, v21 offset1:1
	s_waitcnt vmcnt(10)
	ds_write2_b32 v87, v22, v23 offset1:1
	ds_write2_b32 v88, v24, v25 offset1:1
	s_waitcnt vmcnt(9)
	ds_write2_b32 v89, v26, v27 offset1:1
	ds_write2_b32 v90, v28, v29 offset1:1
	s_waitcnt vmcnt(8)
	ds_write2_b32 v91, v30, v31 offset1:1
	ds_write2_b32 v92, v32, v33 offset1:1
	s_waitcnt lgkmcnt(0)
	ds_read2_b32 v[98:99], v73 offset1:8
	ds_read2_b32 v[100:101], v73 offset0:33 offset1:41
	ds_read2_b32 v[102:103], v73 offset0:66 offset1:74
	ds_read2_b32 v[104:105], v73 offset0:99 offset1:107
	ds_read2_b32 v[106:107], v73 offset0:132 offset1:140
	s_waitcnt lgkmcnt(4)
	v_bfe_u32 v67, v98, 16, 1
	v_add3_u32 v67, v98, v67, s43
	s_waitcnt lgkmcnt(3)
	v_bfe_u32 v93, v100, 16, 1
	v_lshrrev_b32_e32 v67, 16, v67
	v_add3_u32 v93, v100, v93, s43
	ds_read2_b32 v[108:109], v73 offset0:165 offset1:173
	v_and_or_b32 v94, v93, s44, v67
	s_waitcnt lgkmcnt(3)
	v_bfe_u32 v67, v102, 16, 1
	v_add3_u32 v67, v102, v67, s43
	s_waitcnt lgkmcnt(2)
	v_bfe_u32 v93, v104, 16, 1
	ds_read2_b32 v[110:111], v73 offset0:198 offset1:206
	v_lshrrev_b32_e32 v67, 16, v67
	v_add3_u32 v93, v104, v93, s43
	ds_read2_b32 v[112:113], v73 offset0:231 offset1:239
	v_and_or_b32 v95, v93, s44, v67
	s_waitcnt lgkmcnt(3)
	v_bfe_u32 v67, v106, 16, 1
	v_add3_u32 v67, v106, v67, s43
	s_waitcnt lgkmcnt(2)
	v_bfe_u32 v93, v108, 16, 1
	v_lshrrev_b32_e32 v67, 16, v67
	v_add3_u32 v93, v108, v93, s43
	v_and_or_b32 v96, v93, s44, v67
	s_waitcnt lgkmcnt(1)
	v_bfe_u32 v67, v110, 16, 1
	v_add3_u32 v67, v110, v67, s43
	s_waitcnt lgkmcnt(0)
	v_bfe_u32 v93, v112, 16, 1
	s_cmp_eq_u32 s27, 0
	v_lshrrev_b32_e32 v67, 16, v67
	v_add3_u32 v93, v112, v93, s43
	s_cselect_b64 vcc, -1, 0
	s_lshl_b32 s2, s10, 1
	v_and_or_b32 v97, v93, s44, v67
	s_and_b32 s11, s2, 0xffffff00
	v_bitop3_b32 v93, s10, v75, v1 bitop3:0xc8
	v_or_b32_e32 v67, s10, v1
	v_or_b32_e32 v93, s11, v93
	v_cndmask_b32_e32 v67, v93, v67, vcc
	v_add_u32_e32 v67, s37, v67
	v_mad_u64_u32 v[114:115], s[2:3], v67, s36, 0
	v_ashrrev_i32_e32 v93, 31, v67
	v_mov_b32_e32 v98, v115
	v_mad_u64_u32 v[116:117], s[2:3], v93, s36, v[98:99]
	v_mov_b32_e32 v115, v116
	s_ashr_i32 s9, s8, 31
	v_lshl_add_u64 v[114:115], v[114:115], 1, s[6:7]
	s_lshl_b64 s[2:3], s[8:9], 1
	v_bfe_u32 v67, v99, 16, 1
	v_lshl_add_u64 v[114:115], v[114:115], 0, s[2:3]
	v_add3_u32 v67, v99, v67, s43
	v_bfe_u32 v93, v101, 16, 1
	v_lshl_add_u64 v[114:115], v[114:115], 0, v[68:69]
	v_lshrrev_b32_e32 v67, 16, v67
	v_add3_u32 v93, v101, v93, s43
	global_store_dwordx4 v[114:115], v[94:97], off nt
	s_add_i32 s46, s28, s41
	s_cmpk_gt_i32 s46, 0x2fff
	v_and_or_b32 v94, v93, s44, v67
	v_bfe_u32 v67, v103, 16, 1
	v_add3_u32 v67, v103, v67, s43
	v_bfe_u32 v93, v105, 16, 1
	v_lshrrev_b32_e32 v67, 16, v67
	v_add3_u32 v93, v105, v93, s43
	v_and_or_b32 v95, v93, s44, v67
	v_bfe_u32 v67, v107, 16, 1
	v_add3_u32 v67, v107, v67, s43
	v_bfe_u32 v93, v109, 16, 1
	v_lshrrev_b32_e32 v67, 16, v67
	v_add3_u32 v93, v109, v93, s43
	v_and_or_b32 v96, v93, s44, v67
	v_bfe_u32 v67, v111, 16, 1
	v_add3_u32 v67, v111, v67, s43
	v_bfe_u32 v93, v113, 16, 1
	v_lshrrev_b32_e32 v67, 16, v67
	v_add3_u32 v93, v113, v93, s43
	v_and_or_b32 v97, v93, s44, v67
	v_bitop3_b32 v93, s10, v76, v70 bitop3:0xc8
	v_or_b32_e32 v67, s10, v70
	v_or_b32_e32 v93, s11, v93
	v_cndmask_b32_e32 v67, v93, v67, vcc
	v_add_u32_e32 v67, s37, v67
	v_mad_u64_u32 v[98:99], s[24:25], v67, s36, 0
	v_ashrrev_i32_e32 v93, 31, v67
	v_mov_b32_e32 v100, v99
	v_mad_u64_u32 v[100:101], s[24:25], v93, s36, v[100:101]
	v_mov_b32_e32 v99, v100
	v_lshl_add_u64 v[98:99], v[98:99], 1, s[6:7]
	v_lshl_add_u64 v[98:99], v[98:99], 0, s[2:3]
	ds_read2_b32 v[100:101], v73 offset0:16 offset1:24
	v_lshl_add_u64 v[98:99], v[98:99], 0, v[68:69]
	global_store_dwordx4 v[98:99], v[94:97], off nt
	ds_read2_b32 v[98:99], v73 offset0:49 offset1:57
	ds_read2_b32 v[102:103], v73 offset0:82 offset1:90
	ds_read2_b32 v[104:105], v73 offset0:115 offset1:123
	s_waitcnt lgkmcnt(3)
; #define LAS __attribute__((address_space(3)))
; __device__ __forceinline__ unsigned pk2(float lo, float hi) { return f2bf(lo) | (f2bf(hi) << 16); }
;     __device__ __forceinline__ const float* x() const { return (const float*)ld(0); }
;     __device__ __forceinline__ const float* c() const { return (const float*)ld(1); }
; template <bool NT = true> __device__ __forceinline__ void cvt_store(const CvtItem& d, const f32x4 (&v)[8], LAS float* scr, int lane) {
;     ...
;     for (int j = 0; j < 4; ++j) { const int n = (lane >> 3) + 8 * j; const LAS float* s = scr + (8 * c) * 33 + n;
;         u32x4 o; o.x = pk2(s[0 * 33], s[1 * 33]); o.y = pk2(s[2 * 33], s[3 * 33]); o.z = pk2(s[4 * 33], s[5 * 33]); o.w = pk2(s[6 * 33], s[7 * 33]);
;         const int ng = d.n0 + n, drow = d.row_off + (d.ilv ? ((ng >> 7) * 256 + (ng & 127)) : ng);
;         if (NT) __builtin_nontemporal_store(o, (u32x4*)(d.dst + (size_t)drow * d.K + d.k0 + 8 * c)); else *(u32x4*)(d.dst + (size_t)drow * d.K + d.k0 + 8 * c) = o; }
;     asm volatile("s_waitcnt lgkmcnt(0)" ::: "memory");
; __device__ __forceinline__ void convert_moe_items(const Ctx& a, int layer, LAS unsigned char* lds, int it0, int it1, int widx, int nw, int wave, int lane) {
;     ...
;     auto decode = [&](int it) { CvtItem d; const int e = it / PER_E; int r = it % PER_E; const size_t eo = ((size_t)layer * NE + e) * (size_t)DM * FE;
;         if (r < I_G)          { d.src = wg + eo; d.dst = WGU; d.N = FE; d.K = DM; d.row_off = e * 2048; d.ilv = 1; }
;         else if (r < 2 * I_G) { r -= I_G; d.src = wu + eo; d.dst = WGU; d.N = FE; d.K = DM; d.row_off = e * 2048 + 128; d.ilv = 1; }
;         else                  { r -= 2 * I_G; d.src = wd + eo; d.dst = WD; d.N = DM; d.K = FE; d.row_off = e * 2048; d.ilv = 0; }
;         const int nblk = d.N / 32; d.k0 = 64 * (r / nblk); d.n0 = 32 * (r % nblk); return d; };
	v_bfe_u32 v67, v100, 16, 1
	v_add3_u32 v67, v100, v67, s43
	s_waitcnt lgkmcnt(2)
	v_bfe_u32 v93, v98, 16, 1
	ds_read2_b32 v[106:107], v73 offset0:148 offset1:156
	v_lshrrev_b32_e32 v67, 16, v67
	v_add3_u32 v93, v98, v93, s43
	ds_read2_b32 v[108:109], v73 offset0:181 offset1:189
	v_and_or_b32 v94, v93, s44, v67
	s_waitcnt lgkmcnt(3)
	v_bfe_u32 v67, v102, 16, 1
	v_add3_u32 v67, v102, v67, s43
	s_waitcnt lgkmcnt(2)
	v_bfe_u32 v93, v104, 16, 1
	ds_read2_b32 v[110:111], v73 offset0:214 offset1:222
	v_lshrrev_b32_e32 v67, 16, v67
	v_add3_u32 v93, v104, v93, s43
	ds_read2_b32 v[112:113], v73 offset0:247 offset1:255
	v_and_or_b32 v95, v93, s44, v67
	s_waitcnt lgkmcnt(3)
	v_bfe_u32 v67, v106, 16, 1
	v_add3_u32 v67, v106, v67, s43
	s_waitcnt lgkmcnt(2)
	v_bfe_u32 v93, v108, 16, 1
	v_lshrrev_b32_e32 v67, 16, v67
	v_add3_u32 v93, v108, v93, s43
	v_and_or_b32 v96, v93, s44, v67
	s_waitcnt lgkmcnt(1)
	v_bfe_u32 v67, v110, 16, 1
	v_add3_u32 v67, v110, v67, s43
	s_waitcnt lgkmcnt(0)
	v_bfe_u32 v93, v112, 16, 1
	v_lshrrev_b32_e32 v67, 16, v67
	v_add3_u32 v93, v112, v93, s43
	v_and_or_b32 v97, v93, s44, v67
	v_bitop3_b32 v93, s10, v77, v71 bitop3:0xc8
	v_or_b32_e32 v67, s10, v71
	v_or_b32_e32 v93, s11, v93
	v_cndmask_b32_e32 v67, v93, v67, vcc
	v_add_u32_e32 v67, s37, v67
	v_mad_u64_u32 v[114:115], s[24:25], v67, s36, 0
	v_ashrrev_i32_e32 v93, 31, v67
	v_mov_b32_e32 v98, v115
	v_mad_u64_u32 v[116:117], s[24:25], v93, s36, v[98:99]
	v_mov_b32_e32 v115, v116
	v_lshl_add_u64 v[114:115], v[114:115], 1, s[6:7]
	v_bfe_u32 v67, v101, 16, 1
	v_lshl_add_u64 v[114:115], v[114:115], 0, s[2:3]
	v_add3_u32 v67, v101, v67, s43
	v_bfe_u32 v93, v99, 16, 1
	v_lshl_add_u64 v[114:115], v[114:115], 0, v[68:69]
	v_lshrrev_b32_e32 v67, 16, v67
	v_add3_u32 v93, v99, v93, s43
	global_store_dwordx4 v[114:115], v[94:97], off nt
	s_nop 1
	v_and_or_b32 v94, v93, s44, v67
	v_bfe_u32 v67, v103, 16, 1
	v_add3_u32 v67, v103, v67, s43
	v_bfe_u32 v93, v105, 16, 1
	v_lshrrev_b32_e32 v67, 16, v67
	v_add3_u32 v93, v105, v93, s43
	v_and_or_b32 v95, v93, s44, v67
	v_bfe_u32 v67, v107, 16, 1
	v_add3_u32 v67, v107, v67, s43
	v_bfe_u32 v93, v109, 16, 1
	v_lshrrev_b32_e32 v67, 16, v67
	v_add3_u32 v93, v109, v93, s43
	v_and_or_b32 v96, v93, s44, v67
	v_bfe_u32 v67, v111, 16, 1
	v_add3_u32 v67, v111, v67, s43
	v_bfe_u32 v93, v113, 16, 1
	v_lshrrev_b32_e32 v67, 16, v67
	v_add3_u32 v93, v113, v93, s43
	v_and_or_b32 v97, v93, s44, v67
	v_bitop3_b32 v93, s10, v78, v72 bitop3:0xc8
	v_or_b32_e32 v67, s10, v72
	v_or_b32_e32 v93, s11, v93
	v_cndmask_b32_e32 v67, v93, v67, vcc
	v_add_u32_e32 v67, s37, v67
	v_mad_u64_u32 v[98:99], s[24:25], v67, s36, 0
	v_ashrrev_i32_e32 v93, 31, v67
	v_mov_b32_e32 v100, v99
	v_mad_u64_u32 v[100:101], s[24:25], v93, s36, v[100:101]
	v_mov_b32_e32 v99, v100
	v_lshl_add_u64 v[98:99], v[98:99], 1, s[6:7]
	v_lshl_add_u64 v[98:99], v[98:99], 0, s[2:3]
	v_lshl_add_u64 v[98:99], v[98:99], 0, v[68:69]
	global_store_dwordx4 v[98:99], v[94:97], off nt
	s_waitcnt lgkmcnt(0)
	s_cselect_b64 s[24:25], -1, 0
	s_and_b64 vcc, exec, s[24:25]
	s_cbranch_vccnz .LBB0_157
	s_mul_hi_i32 s2, s46, 0x2aaaaaab
	s_lshr_b32 s3, s2, 31
	s_ashr_i32 s2, s2, 9
	s_add_i32 s26, s2, s3
	s_mul_i32 s2, s26, 0xfffff400
	s_ashr_i32 s27, s26, 31
	s_add_i32 s23, s46, s2
	s_lshl_b64 s[8:9], s[26:27], 21
	s_lshl_b32 s47, s26, 11
	s_cmpk_gt_i32 s23, 0x3ff
	s_mov_b64 s[10:11], -1
	s_cbranch_scc0 .LBB0_154
	s_mul_i32 s2, s26, 0xc00
	s_sub_i32 s10, s46, s2
	s_cmpk_gt_u32 s23, 0x7ff
	s_mov_b64 s[6:7], -1
	s_cbranch_scc0 .LBB0_152
	s_add_i32 s21, s10, 0xfffff800
	s_lshl_b64 s[2:3], s[8:9], 2
	s_add_u32 s2, s35, s2
	s_addc_u32 s3, s34, s3
	s_mov_b64 s[6:7], 0

; #define LAS __attribute__((address_space(3)))
; __device__ __forceinline__ unsigned pk2(float lo, float hi) { return f2bf(lo) | (f2bf(hi) << 16); }
;     __device__ __forceinline__ const float* x() const { return (const float*)ld(0); }
;     __device__ __forceinline__ const float* c() const { return (const float*)ld(1); }
; template <bool NT = true> __device__ __forceinline__ void cvt_store(const CvtItem& d, const f32x4 (&v)[8], LAS float* scr, int lane) {
;     const int rr = lane >> 3, c4 = (lane & 7) * 4;
; #pragma unroll
;     for (int q = 0; q < 8; ++q) { LAS float* t = scr + (8 * q + rr) * 33 + c4; t[0] = v[q].x; t[1] = v[q].y; t[2] = v[q].z; t[3] = v[q].w; }
;     asm volatile("s_waitcnt lgkmcnt(0)" ::: "memory");
;     const int c = lane & 7;
; #pragma unroll
;     for (int j = 0; j < 4; ++j) { const int n = (lane >> 3) + 8 * j; const LAS float* s = scr + (8 * c) * 33 + n;
;         u32x4 o; o.x = pk2(s[0 * 33], s[1 * 33]); o.y = pk2(s[2 * 33], s[3 * 33]); o.z = pk2(s[4 * 33], s[5 * 33]); o.w = pk2(s[6 * 33], s[7 * 33]);
;         const int ng = d.n0 + n, drow = d.row_off + (d.ilv ? ((ng >> 7) * 256 + (ng & 127)) : ng);
;         if (NT) __builtin_nontemporal_store(o, (u32x4*)(d.dst + (size_t)drow * d.K + d.k0 + 8 * c)); else *(u32x4*)(d.dst + (size_t)drow * d.K + d.k0 + 8 * c) = o; }
;     asm volatile("s_waitcnt lgkmcnt(0)" ::: "memory");
; }
; __device__ __forceinline__ void convert_moe_items(const Ctx& a, int layer, LAS unsigned char* lds, int it0, int it1, int widx, int nw, int wave, int lane) {
;     ...
;         cvt_store(db, vb, scr, lane);
;         hb = (it + nw < it1);
;         if (hb) { db = decode(it + nw); cvt_load(db, vb, lane); }
.LBB0_158:
	s_cmp_lg_u64 s[24:25], 0
	s_cbranch_scc0 .Lcvt_p0m_m
	s_waitcnt vmcnt(0)
.Lcvt_p0m_m:
	s_waitcnt vmcnt(12)
	ds_write2_b32 v74, v34, v35 offset1:1
	ds_write2_b32 v74, v36, v37 offset0:2 offset1:3
	ds_write2_b32 v79, v38, v39 offset1:1
	ds_write2_b32 v80, v40, v41 offset1:1
	ds_write2_b32 v81, v42, v43 offset1:1
	ds_write2_b32 v82, v44, v45 offset1:1
	ds_write2_b32 v83, v46, v47 offset1:1
	ds_write2_b32 v84, v48, v49 offset1:1
	ds_write2_b32 v85, v50, v51 offset1:1
	ds_write2_b32 v86, v52, v53 offset1:1
	ds_write2_b32 v87, v54, v55 offset1:1
	ds_write2_b32 v88, v56, v57 offset1:1
	ds_write2_b32 v89, v58, v59 offset1:1
	ds_write2_b32 v90, v60, v61 offset1:1
	ds_write2_b32 v91, v62, v63 offset1:1
	ds_write2_b32 v92, v64, v65 offset1:1
	s_waitcnt lgkmcnt(0)
	ds_read2_b32 v[84:85], v73 offset1:8
	ds_read2_b32 v[86:87], v73 offset0:33 offset1:41
	ds_read2_b32 v[88:89], v73 offset0:66 offset1:74
	ds_read2_b32 v[90:91], v73 offset0:99 offset1:107
	ds_read2_b32 v[92:93], v73 offset0:132 offset1:140
	s_waitcnt lgkmcnt(4)
	v_bfe_u32 v67, v84, 16, 1
	v_add3_u32 v67, v84, v67, s43
	s_waitcnt lgkmcnt(3)
	v_bfe_u32 v79, v86, 16, 1
	v_lshrrev_b32_e32 v67, 16, v67
	v_add3_u32 v79, v86, v79, s43
	ds_read2_b32 v[94:95], v73 offset0:165 offset1:173
	v_and_or_b32 v80, v79, s44, v67
	s_waitcnt lgkmcnt(3)
	v_bfe_u32 v67, v88, 16, 1
	v_add3_u32 v67, v88, v67, s43
	s_waitcnt lgkmcnt(2)
	v_bfe_u32 v79, v90, 16, 1
	ds_read2_b32 v[96:97], v73 offset0:198 offset1:206
	v_lshrrev_b32_e32 v67, 16, v67
	v_add3_u32 v79, v90, v79, s43
	ds_read2_b32 v[98:99], v73 offset0:231 offset1:239
	v_and_or_b32 v81, v79, s44, v67
	s_waitcnt lgkmcnt(3)
	v_bfe_u32 v67, v92, 16, 1
	v_add3_u32 v67, v92, v67, s43
	s_waitcnt lgkmcnt(2)
	v_bfe_u32 v79, v94, 16, 1
	v_lshrrev_b32_e32 v67, 16, v67
	v_add3_u32 v79, v94, v79, s43
	v_and_or_b32 v82, v79, s44, v67
	s_waitcnt lgkmcnt(1)
	v_bfe_u32 v67, v96, 16, 1
	v_add3_u32 v67, v96, v67, s43
	s_waitcnt lgkmcnt(0)
	v_bfe_u32 v79, v98, 16, 1
	v_lshrrev_b32_e32 v67, 16, v67
	v_add3_u32 v79, v98, v79, s43
	v_and_or_b32 v83, v79, s44, v67
	v_add_u32_e32 v67, s22, v1
	s_cmp_eq_u32 s38, 0
	v_lshlrev_b32_e32 v79, 1, v67
	v_and_b32_e32 v84, 0x7f, v67
	v_and_or_b32 v79, v79, s45, v84
	s_cselect_b64 vcc, -1, 0
	v_cndmask_b32_e32 v67, v79, v67, vcc
	v_add_u32_e32 v67, s40, v67
	v_mad_u64_u32 v[100:101], s[2:3], v67, s39, 0
	v_ashrrev_i32_e32 v79, 31, v67
	v_mov_b32_e32 v84, v101
	v_mad_u64_u32 v[102:103], s[2:3], v79, s39, v[84:85]
	v_mov_b32_e32 v101, v102
	s_ashr_i32 s21, s20, 31
	v_lshl_add_u64 v[100:101], v[100:101], 1, s[12:13]
	s_lshl_b64 s[2:3], s[20:21], 1
	v_bfe_u32 v67, v85, 16, 1
	v_lshl_add_u64 v[100:101], v[100:101], 0, s[2:3]
	v_add3_u32 v67, v85, v67, s43
	v_bfe_u32 v79, v87, 16, 1
	v_lshl_add_u64 v[100:101], v[100:101], 0, v[68:69]
	v_lshrrev_b32_e32 v67, 16, v67
	v_add3_u32 v79, v87, v79, s43
	global_store_dwordx4 v[100:101], v[80:83], off nt
	s_nop 1
	v_and_or_b32 v80, v79, s44, v67
	v_bfe_u32 v67, v89, 16, 1
	v_add3_u32 v67, v89, v67, s43
	v_bfe_u32 v79, v91, 16, 1
	v_lshrrev_b32_e32 v67, 16, v67
	v_add3_u32 v79, v91, v79, s43
	v_and_or_b32 v81, v79, s44, v67
	v_bfe_u32 v67, v93, 16, 1
	v_add3_u32 v67, v93, v67, s43
	v_bfe_u32 v79, v95, 16, 1
	v_lshrrev_b32_e32 v67, 16, v67
	v_add3_u32 v79, v95, v79, s43
	v_and_or_b32 v82, v79, s44, v67
	v_bfe_u32 v67, v97, 16, 1
	v_add3_u32 v67, v97, v67, s43
	v_bfe_u32 v79, v99, 16, 1
	v_lshrrev_b32_e32 v67, 16, v67
	v_add3_u32 v79, v99, v79, s43
	v_and_or_b32 v83, v79, s44, v67
	v_add_u32_e32 v67, s22, v70
	v_lshlrev_b32_e32 v79, 1, v67
	v_and_b32_e32 v84, 0x7f, v67
	v_and_or_b32 v79, v79, s45, v84
	v_cndmask_b32_e32 v67, v79, v67, vcc
	v_add_u32_e32 v67, s40, v67
	v_mad_u64_u32 v[84:85], s[16:17], v67, s39, 0
	v_ashrrev_i32_e32 v79, 31, v67
	v_mov_b32_e32 v86, v85
	v_mad_u64_u32 v[86:87], s[16:17], v79, s39, v[86:87]
	v_mov_b32_e32 v85, v86
	v_lshl_add_u64 v[84:85], v[84:85], 1, s[12:13]
	v_lshl_add_u64 v[84:85], v[84:85], 0, s[2:3]
	ds_read2_b32 v[86:87], v73 offset0:16 offset1:24
	v_lshl_add_u64 v[84:85], v[84:85], 0, v[68:69]
	global_store_dwordx4 v[84:85], v[80:83], off nt
	ds_read2_b32 v[84:85], v73 offset0:49 offset1:57
	ds_read2_b32 v[88:89], v73 offset0:82 offset1:90
	ds_read2_b32 v[90:91], v73 offset0:115 offset1:123
	s_waitcnt lgkmcnt(3)
; #define LAS __attribute__((address_space(3)))
; __device__ __forceinline__ unsigned pk2(float lo, float hi) { return f2bf(lo) | (f2bf(hi) << 16); }
;     __device__ __forceinline__ const float* x() const { return (const float*)ld(0); }
;     __device__ __forceinline__ const float* c() const { return (const float*)ld(1); }
; template <bool NT = true> __device__ __forceinline__ void cvt_store(const CvtItem& d, const f32x4 (&v)[8], LAS float* scr, int lane) {
;     ...
;     for (int j = 0; j < 4; ++j) { const int n = (lane >> 3) + 8 * j; const LAS float* s = scr + (8 * c) * 33 + n;
;         u32x4 o; o.x = pk2(s[0 * 33], s[1 * 33]); o.y = pk2(s[2 * 33], s[3 * 33]); o.z = pk2(s[4 * 33], s[5 * 33]); o.w = pk2(s[6 * 33], s[7 * 33]);
;         const int ng = d.n0 + n, drow = d.row_off + (d.ilv ? ((ng >> 7) * 256 + (ng & 127)) : ng);
;         if (NT) __builtin_nontemporal_store(o, (u32x4*)(d.dst + (size_t)drow * d.K + d.k0 + 8 * c)); else *(u32x4*)(d.dst + (size_t)drow * d.K + d.k0 + 8 * c) = o; }
;     asm volatile("s_waitcnt lgkmcnt(0)" ::: "memory");
; __device__ __forceinline__ void convert_moe_items(const Ctx& a, int layer, LAS unsigned char* lds, int it0, int it1, int widx, int nw, int wave, int lane) {
;     ...
;     auto decode = [&](int it) { CvtItem d; const int e = it / PER_E; int r = it % PER_E; const size_t eo = ((size_t)layer * NE + e) * (size_t)DM * FE;
;         if (r < I_G)          { d.src = wg + eo; d.dst = WGU; d.N = FE; d.K = DM; d.row_off = e * 2048; d.ilv = 1; }
;         else if (r < 2 * I_G) { r -= I_G; d.src = wu + eo; d.dst = WGU; d.N = FE; d.K = DM; d.row_off = e * 2048 + 128; d.ilv = 1; }
;         else                  { r -= 2 * I_G; d.src = wd + eo; d.dst = WD; d.N = DM; d.K = FE; d.row_off = e * 2048; d.ilv = 0; }
;         const int nblk = d.N / 32; d.k0 = 64 * (r / nblk); d.n0 = 32 * (r % nblk); return d; };
;     ...
;         hb = (it + nw < it1);
;         if (hb) { db = decode(it + nw); cvt_load(db, vb, lane); }
;         if (!ha) break;
;     }
	v_bfe_u32 v67, v86, 16, 1
	v_add3_u32 v67, v86, v67, s43
	s_waitcnt lgkmcnt(2)
	v_bfe_u32 v79, v84, 16, 1
	ds_read2_b32 v[92:93], v73 offset0:148 offset1:156
	v_lshrrev_b32_e32 v67, 16, v67
	v_add3_u32 v79, v84, v79, s43
	ds_read2_b32 v[94:95], v73 offset0:181 offset1:189
	v_and_or_b32 v80, v79, s44, v67
	s_waitcnt lgkmcnt(3)
	v_bfe_u32 v67, v88, 16, 1
	v_add3_u32 v67, v88, v67, s43
	s_waitcnt lgkmcnt(2)
	v_bfe_u32 v79, v90, 16, 1
	ds_read2_b32 v[96:97], v73 offset0:214 offset1:222
	v_lshrrev_b32_e32 v67, 16, v67
	v_add3_u32 v79, v90, v79, s43
	ds_read2_b32 v[98:99], v73 offset0:247 offset1:255
	v_and_or_b32 v81, v79, s44, v67
	s_waitcnt lgkmcnt(3)
	v_bfe_u32 v67, v92, 16, 1
	v_add3_u32 v67, v92, v67, s43
	s_waitcnt lgkmcnt(2)
	v_bfe_u32 v79, v94, 16, 1
	v_lshrrev_b32_e32 v67, 16, v67
	v_add3_u32 v79, v94, v79, s43
	v_and_or_b32 v82, v79, s44, v67
	s_waitcnt lgkmcnt(1)
	v_bfe_u32 v67, v96, 16, 1
	v_add3_u32 v67, v96, v67, s43
	s_waitcnt lgkmcnt(0)
	v_bfe_u32 v79, v98, 16, 1
	v_lshrrev_b32_e32 v67, 16, v67
	v_add3_u32 v79, v98, v79, s43
	v_and_or_b32 v83, v79, s44, v67
	v_add_u32_e32 v67, s22, v71
	v_lshlrev_b32_e32 v79, 1, v67
	v_and_b32_e32 v84, 0x7f, v67
	v_and_or_b32 v79, v79, s45, v84
	v_cndmask_b32_e32 v67, v79, v67, vcc
	v_add_u32_e32 v67, s40, v67
	v_mad_u64_u32 v[100:101], s[16:17], v67, s39, 0
	v_ashrrev_i32_e32 v79, 31, v67
	v_mov_b32_e32 v84, v101
	v_mad_u64_u32 v[102:103], s[16:17], v79, s39, v[84:85]
	v_mov_b32_e32 v101, v102
	v_lshl_add_u64 v[100:101], v[100:101], 1, s[12:13]
	v_bfe_u32 v67, v87, 16, 1
	v_lshl_add_u64 v[100:101], v[100:101], 0, s[2:3]
	v_add3_u32 v67, v87, v67, s43
	v_bfe_u32 v79, v85, 16, 1
	v_lshl_add_u64 v[100:101], v[100:101], 0, v[68:69]
	v_lshrrev_b32_e32 v67, 16, v67
	v_add3_u32 v79, v85, v79, s43
	global_store_dwordx4 v[100:101], v[80:83], off nt
	s_nop 1
	v_and_or_b32 v80, v79, s44, v67
	v_bfe_u32 v67, v89, 16, 1
	v_add3_u32 v67, v89, v67, s43
	v_bfe_u32 v79, v91, 16, 1
	v_lshrrev_b32_e32 v67, 16, v67
	v_add3_u32 v79, v91, v79, s43
	v_and_or_b32 v81, v79, s44, v67
	v_bfe_u32 v67, v93, 16, 1
	v_add3_u32 v67, v93, v67, s43
	v_bfe_u32 v79, v95, 16, 1
	v_lshrrev_b32_e32 v67, 16, v67
	v_add3_u32 v79, v95, v79, s43
	v_and_or_b32 v82, v79, s44, v67
	v_bfe_u32 v67, v97, 16, 1
	v_add3_u32 v67, v97, v67, s43
	v_bfe_u32 v79, v99, 16, 1
	v_lshrrev_b32_e32 v67, 16, v67
	v_add3_u32 v79, v99, v79, s43
	v_and_or_b32 v83, v79, s44, v67
	v_add_u32_e32 v67, s22, v72
	v_lshlrev_b32_e32 v79, 1, v67
	v_and_b32_e32 v84, 0x7f, v67
	v_and_or_b32 v79, v79, s45, v84
	v_cndmask_b32_e32 v67, v79, v67, vcc
	v_add_u32_e32 v67, s40, v67
	v_mad_u64_u32 v[84:85], s[16:17], v67, s39, 0
	v_ashrrev_i32_e32 v79, 31, v67
	v_mov_b32_e32 v86, v85
	v_mad_u64_u32 v[86:87], s[16:17], v79, s39, v[86:87]
	v_mov_b32_e32 v85, v86
	v_lshl_add_u64 v[84:85], v[84:85], 1, s[12:13]
	v_lshl_add_u64 v[84:85], v[84:85], 0, s[2:3]
	v_lshl_add_u64 v[84:85], v[84:85], 0, v[68:69]
	global_store_dwordx4 v[84:85], v[80:83], off nt
	s_add_i32 s2, s42, s28
	s_waitcnt lgkmcnt(0)
	s_cmpk_lt_i32 s2, 0x3000
	s_cselect_b64 s[16:17], -1, 0
	s_cmpk_gt_i32 s2, 0x2fff
	s_cbranch_scc1 .LBB0_146
	s_mul_hi_i32 s3, s2, 0x2aaaaaab
	s_lshr_b32 s9, s3, 31
	s_ashr_i32 s3, s3, 9
	s_add_i32 s12, s3, s9
	s_mul_i32 s3, s12, 0xc00
	s_ashr_i32 s13, s12, 31
	s_sub_i32 s11, s2, s3
	s_lshl_b64 s[20:21], s[12:13], 21
	s_lshl_b32 s26, s12, 11
	s_cmpk_gt_i32 s11, 0x3ff
	s_mov_b64 s[22:23], -1
	s_cbranch_scc0 .LBB0_164
	s_cmpk_gt_u32 s11, 0x7ff
	s_mov_b64 s[12:13], -1
	s_cbranch_scc0 .LBB0_162
	s_add_i32 s9, s11, 0xfffff800
	s_lshl_b64 s[2:3], s[20:21], 2
	s_add_u32 s2, s35, s2
	s_addc_u32 s3, s34, s3
	s_mov_b64 s[12:13], 0

; #define LAS __attribute__((address_space(3)))
; __device__ __forceinline__ unsigned pk2(float lo, float hi) { return f2bf(lo) | (f2bf(hi) << 16); }
;     __device__ __forceinline__ const float* x() const { return (const float*)ld(0); }
;     __device__ __forceinline__ const float* c() const { return (const float*)ld(1); }
; template <bool NT = true> __device__ __forceinline__ void cvt_store(const CvtItem& d, const f32x4 (&v)[8], LAS float* scr, int lane) {
;     const int rr = lane >> 3, c4 = (lane & 7) * 4;
; #pragma unroll
;     for (int q = 0; q < 8; ++q) { LAS float* t = scr + (8 * q + rr) * 33 + c4; t[0] = v[q].x; t[1] = v[q].y; t[2] = v[q].z; t[3] = v[q].w; }
;     asm volatile("s_waitcnt lgkmcnt(0)" ::: "memory");
;     const int c = lane & 7;
; #pragma unroll
;     for (int j = 0; j < 4; ++j) { const int n = (lane >> 3) + 8 * j; const LAS float* s = scr + (8 * c) * 33 + n;
;         u32x4 o; o.x = pk2(s[0 * 33], s[1 * 33]); o.y = pk2(s[2 * 33], s[3 * 33]); o.z = pk2(s[4 * 33], s[5 * 33]); o.w = pk2(s[6 * 33], s[7 * 33]);
;         const int ng = d.n0 + n, drow = d.row_off + (d.ilv ? ((ng >> 7) * 256 + (ng & 127)) : ng);
;         if (NT) __builtin_nontemporal_store(o, (u32x4*)(d.dst + (size_t)drow * d.K + d.k0 + 8 * c)); else *(u32x4*)(d.dst + (size_t)drow * d.K + d.k0 + 8 * c) = o; }
;     asm volatile("s_waitcnt lgkmcnt(0)" ::: "memory");
; }
; __device__ __forceinline__ void convert_moe_items(const Ctx& a, int layer, LAS unsigned char* lds, int it0, int it1, int widx, int nw, int wave, int lane) {
;     ...
;     for (;;) {
;         cvt_store(da, va, scr, lane);
;         it += 2 * nw; const bool ha = (it < it1);
;         if (ha) { da = decode(it); cvt_load(da, va, lane); }
.Lcvt_p2b_t:
	v_add_u32_e32 v79, 0x420, v74
	v_add_u32_e32 v80, 0x428, v74
	v_add_u32_e32 v81, 0x840, v74
	v_add_u32_e32 v82, 0x848, v74
	v_add_u32_e32 v83, 0xc60, v74
	v_add_u32_e32 v84, 0xc68, v74
	v_add_u32_e32 v85, 0x1080, v74
	v_add_u32_e32 v86, 0x1088, v74
	v_add_u32_e32 v87, 0x14a0, v74
	v_add_u32_e32 v88, 0x14a8, v74
	v_add_u32_e32 v89, 0x18c0, v74
	v_add_u32_e32 v90, 0x18c8, v74
	v_add_u32_e32 v91, 0x1ce0, v74
	v_add_u32_e32 v92, 0x1ce8, v74
	s_waitcnt vmcnt(15)
	ds_write2_b32 v74, v2, v3 offset1:1
	ds_write2_b32 v74, v4, v5 offset0:2 offset1:3
	s_waitcnt vmcnt(14)
	ds_write2_b32 v79, v6, v7 offset1:1
	ds_write2_b32 v80, v8, v9 offset1:1
	s_waitcnt vmcnt(13)
	ds_write2_b32 v81, v10, v11 offset1:1
	ds_write2_b32 v82, v12, v13 offset1:1
	s_waitcnt vmcnt(12)
	ds_write2_b32 v83, v14, v15 offset1:1
	ds_write2_b32 v84, v16, v17 offset1:1
	s_waitcnt vmcnt(11)
	ds_write2_b32 v85, v18, v19 offset1:1
	ds_write2_b32 v86, v20, v21 offset1:1
	s_waitcnt vmcnt(10)
	ds_write2_b32 v87, v22, v23 offset1:1
	ds_write2_b32 v88, v24, v25 offset1:1
	s_waitcnt vmcnt(9)
	ds_write2_b32 v89, v26, v27 offset1:1
	ds_write2_b32 v90, v28, v29 offset1:1
	s_waitcnt vmcnt(8)
	ds_write2_b32 v91, v30, v31 offset1:1
	ds_write2_b32 v92, v32, v33 offset1:1
	s_waitcnt lgkmcnt(0)
	ds_read2_b32 v[98:99], v73 offset1:8
	ds_read2_b32 v[100:101], v73 offset0:33 offset1:41
	ds_read2_b32 v[102:103], v73 offset0:66 offset1:74
	ds_read2_b32 v[104:105], v73 offset0:99 offset1:107
	ds_read2_b32 v[106:107], v73 offset0:132 offset1:140
	s_waitcnt lgkmcnt(4)
	v_bfe_u32 v67, v98, 16, 1
	v_add3_u32 v67, v98, v67, s43
	s_waitcnt lgkmcnt(3)
	v_bfe_u32 v93, v100, 16, 1
	v_lshrrev_b32_e32 v67, 16, v67
	v_add3_u32 v93, v100, v93, s43
	ds_read2_b32 v[108:109], v73 offset0:165 offset1:173
	v_and_or_b32 v94, v93, s44, v67
	s_waitcnt lgkmcnt(3)
	v_bfe_u32 v67, v102, 16, 1
	v_add3_u32 v67, v102, v67, s43
	s_waitcnt lgkmcnt(2)
	v_bfe_u32 v93, v104, 16, 1
	ds_read2_b32 v[110:111], v73 offset0:198 offset1:206
	v_lshrrev_b32_e32 v67, 16, v67
	v_add3_u32 v93, v104, v93, s43
	ds_read2_b32 v[112:113], v73 offset0:231 offset1:239
	v_and_or_b32 v95, v93, s44, v67
	s_waitcnt lgkmcnt(3)
	v_bfe_u32 v67, v106, 16, 1
	v_add3_u32 v67, v106, v67, s43
	s_waitcnt lgkmcnt(2)
	v_bfe_u32 v93, v108, 16, 1
	v_lshrrev_b32_e32 v67, 16, v67
	v_add3_u32 v93, v108, v93, s43
	v_and_or_b32 v96, v93, s44, v67
	s_waitcnt lgkmcnt(1)
	v_bfe_u32 v67, v110, 16, 1
	v_add3_u32 v67, v110, v67, s43
	s_waitcnt lgkmcnt(0)
	v_bfe_u32 v93, v112, 16, 1
	s_cmp_eq_u32 s27, 0
	v_lshrrev_b32_e32 v67, 16, v67
	v_add3_u32 v93, v112, v93, s43
	s_cselect_b64 vcc, -1, 0
	s_lshl_b32 s2, s10, 1
	v_and_or_b32 v97, v93, s44, v67
	s_and_b32 s11, s2, 0xffffff00
	v_bitop3_b32 v93, s10, v75, v70 bitop3:0xc8
	v_or_b32_e32 v67, s10, v70
	v_or_b32_e32 v93, s11, v93
	v_cndmask_b32_e32 v67, v93, v67, vcc
	v_add_u32_e32 v67, s38, v67
	v_mad_u64_u32 v[114:115], s[2:3], v67, s37, 0
	v_ashrrev_i32_e32 v93, 31, v67
	v_mov_b32_e32 v98, v115
	v_mad_u64_u32 v[116:117], s[2:3], v93, s37, v[98:99]
	v_mov_b32_e32 v115, v116
	s_ashr_i32 s9, s8, 31
	v_lshl_add_u64 v[114:115], v[114:115], 1, s[6:7]
	s_lshl_b64 s[2:3], s[8:9], 1
	v_bfe_u32 v67, v99, 16, 1
	v_lshl_add_u64 v[114:115], v[114:115], 0, s[2:3]
	v_add3_u32 v67, v99, v67, s43
	v_bfe_u32 v93, v101, 16, 1
	v_lshl_add_u64 v[114:115], v[114:115], 0, v[68:69]
	v_lshrrev_b32_e32 v67, 16, v67
	v_add3_u32 v93, v101, v93, s43
	global_store_dwordx4 v[114:115], v[94:97], off nt
	s_add_i32 s46, s39, s42
	s_cmp_gt_i32 s46, 0xbfff
	v_and_or_b32 v94, v93, s44, v67
	v_bfe_u32 v67, v103, 16, 1
	v_add3_u32 v67, v103, v67, s43
	v_bfe_u32 v93, v105, 16, 1
	v_lshrrev_b32_e32 v67, 16, v67
	v_add3_u32 v93, v105, v93, s43
	v_and_or_b32 v95, v93, s44, v67
	v_bfe_u32 v67, v107, 16, 1
	v_add3_u32 v67, v107, v67, s43
	v_bfe_u32 v93, v109, 16, 1
	v_lshrrev_b32_e32 v67, 16, v67
	v_add3_u32 v93, v109, v93, s43
	v_and_or_b32 v96, v93, s44, v67
	v_bfe_u32 v67, v111, 16, 1
	v_add3_u32 v67, v111, v67, s43
	v_bfe_u32 v93, v113, 16, 1
	v_lshrrev_b32_e32 v67, 16, v67
	v_add3_u32 v93, v113, v93, s43
	v_and_or_b32 v97, v93, s44, v67
	v_bitop3_b32 v93, s10, v76, v1 bitop3:0xc8
	v_or_b32_e32 v67, s10, v1
	v_or_b32_e32 v93, s11, v93
	v_cndmask_b32_e32 v67, v93, v67, vcc
	v_add_u32_e32 v67, s38, v67
	v_mad_u64_u32 v[98:99], s[24:25], v67, s37, 0
	v_ashrrev_i32_e32 v93, 31, v67
	v_mov_b32_e32 v100, v99
	v_mad_u64_u32 v[100:101], s[24:25], v93, s37, v[100:101]
	v_mov_b32_e32 v99, v100
	v_lshl_add_u64 v[98:99], v[98:99], 1, s[6:7]
	v_lshl_add_u64 v[98:99], v[98:99], 0, s[2:3]
	ds_read2_b32 v[100:101], v73 offset0:16 offset1:24
	v_lshl_add_u64 v[98:99], v[98:99], 0, v[68:69]
	global_store_dwordx4 v[98:99], v[94:97], off nt
	ds_read2_b32 v[98:99], v73 offset0:49 offset1:57
	ds_read2_b32 v[102:103], v73 offset0:82 offset1:90
	ds_read2_b32 v[104:105], v73 offset0:115 offset1:123
	s_waitcnt lgkmcnt(3)
; #define LAS __attribute__((address_space(3)))
; __device__ __forceinline__ unsigned pk2(float lo, float hi) { return f2bf(lo) | (f2bf(hi) << 16); }
;     __device__ __forceinline__ const float* x() const { return (const float*)ld(0); }
;     __device__ __forceinline__ const float* c() const { return (const float*)ld(1); }
; template <bool NT = true> __device__ __forceinline__ void cvt_store(const CvtItem& d, const f32x4 (&v)[8], LAS float* scr, int lane) {
;     ...
;     for (int j = 0; j < 4; ++j) { const int n = (lane >> 3) + 8 * j; const LAS float* s = scr + (8 * c) * 33 + n;
;         u32x4 o; o.x = pk2(s[0 * 33], s[1 * 33]); o.y = pk2(s[2 * 33], s[3 * 33]); o.z = pk2(s[4 * 33], s[5 * 33]); o.w = pk2(s[6 * 33], s[7 * 33]);
;         const int ng = d.n0 + n, drow = d.row_off + (d.ilv ? ((ng >> 7) * 256 + (ng & 127)) : ng);
;         if (NT) __builtin_nontemporal_store(o, (u32x4*)(d.dst + (size_t)drow * d.K + d.k0 + 8 * c)); else *(u32x4*)(d.dst + (size_t)drow * d.K + d.k0 + 8 * c) = o; }
;     asm volatile("s_waitcnt lgkmcnt(0)" ::: "memory");
; __device__ __forceinline__ void convert_moe_items(const Ctx& a, int layer, LAS unsigned char* lds, int it0, int it1, int widx, int nw, int wave, int lane) {
;     ...
;     auto decode = [&](int it) { CvtItem d; const int e = it / PER_E; int r = it % PER_E; const size_t eo = ((size_t)layer * NE + e) * (size_t)DM * FE;
;         if (r < I_G)          { d.src = wg + eo; d.dst = WGU; d.N = FE; d.K = DM; d.row_off = e * 2048; d.ilv = 1; }
;         else if (r < 2 * I_G) { r -= I_G; d.src = wu + eo; d.dst = WGU; d.N = FE; d.K = DM; d.row_off = e * 2048 + 128; d.ilv = 1; }
;         else                  { r -= 2 * I_G; d.src = wd + eo; d.dst = WD; d.N = DM; d.K = FE; d.row_off = e * 2048; d.ilv = 0; }
;         const int nblk = d.N / 32; d.k0 = 64 * (r / nblk); d.n0 = 32 * (r % nblk); return d; };
	v_bfe_u32 v67, v100, 16, 1
	v_add3_u32 v67, v100, v67, s43
	s_waitcnt lgkmcnt(2)
	v_bfe_u32 v93, v98, 16, 1
	ds_read2_b32 v[106:107], v73 offset0:148 offset1:156
	v_lshrrev_b32_e32 v67, 16, v67
	v_add3_u32 v93, v98, v93, s43
	ds_read2_b32 v[108:109], v73 offset0:181 offset1:189
	v_and_or_b32 v94, v93, s44, v67
	s_waitcnt lgkmcnt(3)
	v_bfe_u32 v67, v102, 16, 1
	v_add3_u32 v67, v102, v67, s43
	s_waitcnt lgkmcnt(2)
	v_bfe_u32 v93, v104, 16, 1
	ds_read2_b32 v[110:111], v73 offset0:214 offset1:222
	v_lshrrev_b32_e32 v67, 16, v67
	v_add3_u32 v93, v104, v93, s43
	ds_read2_b32 v[112:113], v73 offset0:247 offset1:255
	v_and_or_b32 v95, v93, s44, v67
	s_waitcnt lgkmcnt(3)
	v_bfe_u32 v67, v106, 16, 1
	v_add3_u32 v67, v106, v67, s43
	s_waitcnt lgkmcnt(2)
	v_bfe_u32 v93, v108, 16, 1
	v_lshrrev_b32_e32 v67, 16, v67
	v_add3_u32 v93, v108, v93, s43
	v_and_or_b32 v96, v93, s44, v67
	s_waitcnt lgkmcnt(1)
	v_bfe_u32 v67, v110, 16, 1
	v_add3_u32 v67, v110, v67, s43
	s_waitcnt lgkmcnt(0)
	v_bfe_u32 v93, v112, 16, 1
	v_lshrrev_b32_e32 v67, 16, v67
	v_add3_u32 v93, v112, v93, s43
	v_and_or_b32 v97, v93, s44, v67
	v_bitop3_b32 v93, s10, v77, v71 bitop3:0xc8
	v_or_b32_e32 v67, s10, v71
	v_or_b32_e32 v93, s11, v93
	v_cndmask_b32_e32 v67, v93, v67, vcc
	v_add_u32_e32 v67, s38, v67
	v_mad_u64_u32 v[114:115], s[24:25], v67, s37, 0
	v_ashrrev_i32_e32 v93, 31, v67
	v_mov_b32_e32 v98, v115
	v_mad_u64_u32 v[116:117], s[24:25], v93, s37, v[98:99]
	v_mov_b32_e32 v115, v116
	v_lshl_add_u64 v[114:115], v[114:115], 1, s[6:7]
	v_bfe_u32 v67, v101, 16, 1
	v_lshl_add_u64 v[114:115], v[114:115], 0, s[2:3]
	v_add3_u32 v67, v101, v67, s43
	v_bfe_u32 v93, v99, 16, 1
	v_lshl_add_u64 v[114:115], v[114:115], 0, v[68:69]
	v_lshrrev_b32_e32 v67, 16, v67
	v_add3_u32 v93, v99, v93, s43
	global_store_dwordx4 v[114:115], v[94:97], off nt
	s_nop 1
	v_and_or_b32 v94, v93, s44, v67
	v_bfe_u32 v67, v103, 16, 1
	v_add3_u32 v67, v103, v67, s43
	v_bfe_u32 v93, v105, 16, 1
	v_lshrrev_b32_e32 v67, 16, v67
	v_add3_u32 v93, v105, v93, s43
	v_and_or_b32 v95, v93, s44, v67
	v_bfe_u32 v67, v107, 16, 1
	v_add3_u32 v67, v107, v67, s43
	v_bfe_u32 v93, v109, 16, 1
	v_lshrrev_b32_e32 v67, 16, v67
	v_add3_u32 v93, v109, v93, s43
	v_and_or_b32 v96, v93, s44, v67
	v_bfe_u32 v67, v111, 16, 1
	v_add3_u32 v67, v111, v67, s43
	v_bfe_u32 v93, v113, 16, 1
	v_lshrrev_b32_e32 v67, 16, v67
	v_add3_u32 v93, v113, v93, s43
	v_and_or_b32 v97, v93, s44, v67
	v_bitop3_b32 v93, s10, v78, v72 bitop3:0xc8
	v_or_b32_e32 v67, s10, v72
	v_or_b32_e32 v93, s11, v93
	v_cndmask_b32_e32 v67, v93, v67, vcc
	v_add_u32_e32 v67, s38, v67
	v_mad_u64_u32 v[98:99], s[24:25], v67, s37, 0
	v_ashrrev_i32_e32 v93, 31, v67
	v_mov_b32_e32 v100, v99
	v_mad_u64_u32 v[100:101], s[24:25], v93, s37, v[100:101]
	v_mov_b32_e32 v99, v100
	v_lshl_add_u64 v[98:99], v[98:99], 1, s[6:7]
	v_lshl_add_u64 v[98:99], v[98:99], 0, s[2:3]
	v_lshl_add_u64 v[98:99], v[98:99], 0, v[68:69]
	global_store_dwordx4 v[98:99], v[94:97], off nt
	s_waitcnt lgkmcnt(0)
	s_cselect_b64 s[24:25], -1, 0
	s_and_b64 vcc, exec, s[24:25]
	s_cbranch_vccnz .LBB0_460
	s_mul_hi_i32 s2, s46, 0x2aaaaaab
	s_lshr_b32 s3, s2, 31
	s_ashr_i32 s2, s2, 9
	s_add_i32 s26, s2, s3
	s_mul_i32 s2, s26, 0xfffff400
	s_ashr_i32 s27, s26, 31
	s_add_i32 s23, s46, s2
	s_lshl_b64 s[8:9], s[26:27], 21
	s_lshl_b32 s47, s26, 11
	s_cmpk_gt_i32 s23, 0x3ff
	s_mov_b64 s[10:11], -1
	s_cbranch_scc0 .LBB0_457
	s_mul_i32 s2, s26, 0xc00
	s_sub_i32 s10, s46, s2
	s_cmpk_gt_u32 s23, 0x7ff
	s_mov_b64 s[6:7], -1
	s_cbranch_scc0 .LBB0_455
	s_add_i32 s21, s10, 0xfffff800
	s_lshl_b64 s[2:3], s[8:9], 2
	s_add_u32 s2, s36, s2
	s_addc_u32 s3, s35, s3
	s_mov_b64 s[6:7], 0

; #define LAS __attribute__((address_space(3)))
; __device__ __forceinline__ unsigned pk2(float lo, float hi) { return f2bf(lo) | (f2bf(hi) << 16); }
;     __device__ __forceinline__ const float* x() const { return (const float*)ld(0); }
;     __device__ __forceinline__ const float* c() const { return (const float*)ld(1); }
; template <bool NT = true> __device__ __forceinline__ void cvt_store(const CvtItem& d, const f32x4 (&v)[8], LAS float* scr, int lane) {
;     const int rr = lane >> 3, c4 = (lane & 7) * 4;
; #pragma unroll
;     for (int q = 0; q < 8; ++q) { LAS float* t = scr + (8 * q + rr) * 33 + c4; t[0] = v[q].x; t[1] = v[q].y; t[2] = v[q].z; t[3] = v[q].w; }
;     asm volatile("s_waitcnt lgkmcnt(0)" ::: "memory");
;     const int c = lane & 7;
; #pragma unroll
;     for (int j = 0; j < 4; ++j) { const int n = (lane >> 3) + 8 * j; const LAS float* s = scr + (8 * c) * 33 + n;
;         u32x4 o; o.x = pk2(s[0 * 33], s[1 * 33]); o.y = pk2(s[2 * 33], s[3 * 33]); o.z = pk2(s[4 * 33], s[5 * 33]); o.w = pk2(s[6 * 33], s[7 * 33]);
;         const int ng = d.n0 + n, drow = d.row_off + (d.ilv ? ((ng >> 7) * 256 + (ng & 127)) : ng);
;         if (NT) __builtin_nontemporal_store(o, (u32x4*)(d.dst + (size_t)drow * d.K + d.k0 + 8 * c)); else *(u32x4*)(d.dst + (size_t)drow * d.K + d.k0 + 8 * c) = o; }
;     asm volatile("s_waitcnt lgkmcnt(0)" ::: "memory");
; }
; __device__ __forceinline__ void convert_moe_items(const Ctx& a, int layer, LAS unsigned char* lds, int it0, int it1, int widx, int nw, int wave, int lane) {
;     ...
;         cvt_store(db, vb, scr, lane);
;         hb = (it + nw < it1);
;         if (hb) { db = decode(it + nw); cvt_load(db, vb, lane); }
.Lcvt_p2b_m:
	s_waitcnt vmcnt(12)
	ds_write2_b32 v74, v34, v35 offset1:1
	ds_write2_b32 v74, v36, v37 offset0:2 offset1:3
	ds_write2_b32 v79, v38, v39 offset1:1
	ds_write2_b32 v80, v40, v41 offset1:1
	ds_write2_b32 v81, v42, v43 offset1:1
	ds_write2_b32 v82, v44, v45 offset1:1
	ds_write2_b32 v83, v46, v47 offset1:1
	ds_write2_b32 v84, v48, v49 offset1:1
	ds_write2_b32 v85, v50, v51 offset1:1
	ds_write2_b32 v86, v52, v53 offset1:1
	ds_write2_b32 v87, v54, v55 offset1:1
	ds_write2_b32 v88, v56, v57 offset1:1
	ds_write2_b32 v89, v58, v59 offset1:1
	ds_write2_b32 v90, v60, v61 offset1:1
	ds_write2_b32 v91, v62, v63 offset1:1
	ds_write2_b32 v92, v64, v65 offset1:1
	s_waitcnt lgkmcnt(0)
	ds_read2_b32 v[84:85], v73 offset1:8
	ds_read2_b32 v[86:87], v73 offset0:33 offset1:41
	ds_read2_b32 v[88:89], v73 offset0:66 offset1:74
	ds_read2_b32 v[90:91], v73 offset0:99 offset1:107
	ds_read2_b32 v[92:93], v73 offset0:132 offset1:140
	s_waitcnt lgkmcnt(4)
	v_bfe_u32 v67, v84, 16, 1
	v_add3_u32 v67, v84, v67, s43
	s_waitcnt lgkmcnt(3)
	v_bfe_u32 v79, v86, 16, 1
	v_lshrrev_b32_e32 v67, 16, v67
	v_add3_u32 v79, v86, v79, s43
	ds_read2_b32 v[94:95], v73 offset0:165 offset1:173
	v_and_or_b32 v80, v79, s44, v67
	s_waitcnt lgkmcnt(3)
	v_bfe_u32 v67, v88, 16, 1
	v_add3_u32 v67, v88, v67, s43
	s_waitcnt lgkmcnt(2)
	v_bfe_u32 v79, v90, 16, 1
	ds_read2_b32 v[96:97], v73 offset0:198 offset1:206
	v_lshrrev_b32_e32 v67, 16, v67
	v_add3_u32 v79, v90, v79, s43
	ds_read2_b32 v[98:99], v73 offset0:231 offset1:239
	v_and_or_b32 v81, v79, s44, v67
	s_waitcnt lgkmcnt(3)
	v_bfe_u32 v67, v92, 16, 1
	v_add3_u32 v67, v92, v67, s43
	s_waitcnt lgkmcnt(2)
	v_bfe_u32 v79, v94, 16, 1
	v_lshrrev_b32_e32 v67, 16, v67
	v_add3_u32 v79, v94, v79, s43
	v_and_or_b32 v82, v79, s44, v67
	s_waitcnt lgkmcnt(1)
	v_bfe_u32 v67, v96, 16, 1
	v_add3_u32 v67, v96, v67, s43
	s_waitcnt lgkmcnt(0)
	v_bfe_u32 v79, v98, 16, 1
	v_lshrrev_b32_e32 v67, 16, v67
	v_add3_u32 v79, v98, v79, s43
	v_and_or_b32 v83, v79, s44, v67
	v_add_u32_e32 v67, s22, v70
	s_cmp_eq_u32 s29, 0
	v_lshlrev_b32_e32 v79, 1, v67
	v_and_b32_e32 v84, 0x7f, v67
	v_and_or_b32 v79, v79, s45, v84
	s_cselect_b64 vcc, -1, 0
	v_cndmask_b32_e32 v67, v79, v67, vcc
	v_add_u32_e32 v67, s41, v67
	v_mad_u64_u32 v[100:101], s[2:3], v67, s40, 0
	v_ashrrev_i32_e32 v79, 31, v67
	v_mov_b32_e32 v84, v101
	v_mad_u64_u32 v[102:103], s[2:3], v79, s40, v[84:85]
	v_mov_b32_e32 v101, v102
	s_ashr_i32 s21, s20, 31
	v_lshl_add_u64 v[100:101], v[100:101], 1, s[12:13]
	s_lshl_b64 s[2:3], s[20:21], 1
	v_bfe_u32 v67, v85, 16, 1
	v_lshl_add_u64 v[100:101], v[100:101], 0, s[2:3]
	v_add3_u32 v67, v85, v67, s43
	v_bfe_u32 v79, v87, 16, 1
	v_lshl_add_u64 v[100:101], v[100:101], 0, v[68:69]
	v_lshrrev_b32_e32 v67, 16, v67
	v_add3_u32 v79, v87, v79, s43
	global_store_dwordx4 v[100:101], v[80:83], off nt
	s_nop 1
	v_and_or_b32 v80, v79, s44, v67
	v_bfe_u32 v67, v89, 16, 1
	v_add3_u32 v67, v89, v67, s43
	v_bfe_u32 v79, v91, 16, 1
	v_lshrrev_b32_e32 v67, 16, v67
	v_add3_u32 v79, v91, v79, s43
	v_and_or_b32 v81, v79, s44, v67
	v_bfe_u32 v67, v93, 16, 1
	v_add3_u32 v67, v93, v67, s43
	v_bfe_u32 v79, v95, 16, 1
	v_lshrrev_b32_e32 v67, 16, v67
	v_add3_u32 v79, v95, v79, s43
	v_and_or_b32 v82, v79, s44, v67
	v_bfe_u32 v67, v97, 16, 1
	v_add3_u32 v67, v97, v67, s43
	v_bfe_u32 v79, v99, 16, 1
	v_lshrrev_b32_e32 v67, 16, v67
	v_add3_u32 v79, v99, v79, s43
	v_and_or_b32 v83, v79, s44, v67
	v_add_u32_e32 v67, s22, v1
	v_lshlrev_b32_e32 v79, 1, v67
	v_and_b32_e32 v84, 0x7f, v67
	v_and_or_b32 v79, v79, s45, v84
	v_cndmask_b32_e32 v67, v79, v67, vcc
	v_add_u32_e32 v67, s41, v67
	v_mad_u64_u32 v[84:85], s[16:17], v67, s40, 0
	v_ashrrev_i32_e32 v79, 31, v67
	v_mov_b32_e32 v86, v85
	v_mad_u64_u32 v[86:87], s[16:17], v79, s40, v[86:87]
	v_mov_b32_e32 v85, v86
	v_lshl_add_u64 v[84:85], v[84:85], 1, s[12:13]
	v_lshl_add_u64 v[84:85], v[84:85], 0, s[2:3]
	ds_read2_b32 v[86:87], v73 offset0:16 offset1:24
	v_lshl_add_u64 v[84:85], v[84:85], 0, v[68:69]
	global_store_dwordx4 v[84:85], v[80:83], off nt
	ds_read2_b32 v[84:85], v73 offset0:49 offset1:57
	ds_read2_b32 v[88:89], v73 offset0:82 offset1:90
	ds_read2_b32 v[90:91], v73 offset0:115 offset1:123
	s_waitcnt lgkmcnt(3)
; #define LAS __attribute__((address_space(3)))
; __device__ __forceinline__ unsigned pk2(float lo, float hi) { return f2bf(lo) | (f2bf(hi) << 16); }
;     __device__ __forceinline__ const float* x() const { return (const float*)ld(0); }
;     __device__ __forceinline__ const float* c() const { return (const float*)ld(1); }
; template <bool NT = true> __device__ __forceinline__ void cvt_store(const CvtItem& d, const f32x4 (&v)[8], LAS float* scr, int lane) {
;     ...
;     for (int j = 0; j < 4; ++j) { const int n = (lane >> 3) + 8 * j; const LAS float* s = scr + (8 * c) * 33 + n;
;         u32x4 o; o.x = pk2(s[0 * 33], s[1 * 33]); o.y = pk2(s[2 * 33], s[3 * 33]); o.z = pk2(s[4 * 33], s[5 * 33]); o.w = pk2(s[6 * 33], s[7 * 33]);
;         const int ng = d.n0 + n, drow = d.row_off + (d.ilv ? ((ng >> 7) * 256 + (ng & 127)) : ng);
;         if (NT) __builtin_nontemporal_store(o, (u32x4*)(d.dst + (size_t)drow * d.K + d.k0 + 8 * c)); else *(u32x4*)(d.dst + (size_t)drow * d.K + d.k0 + 8 * c) = o; }
;     asm volatile("s_waitcnt lgkmcnt(0)" ::: "memory");
; __device__ __forceinline__ void convert_moe_items(const Ctx& a, int layer, LAS unsigned char* lds, int it0, int it1, int widx, int nw, int wave, int lane) {
;     ...
;     auto decode = [&](int it) { CvtItem d; const int e = it / PER_E; int r = it % PER_E; const size_t eo = ((size_t)layer * NE + e) * (size_t)DM * FE;
;         if (r < I_G)          { d.src = wg + eo; d.dst = WGU; d.N = FE; d.K = DM; d.row_off = e * 2048; d.ilv = 1; }
;         else if (r < 2 * I_G) { r -= I_G; d.src = wu + eo; d.dst = WGU; d.N = FE; d.K = DM; d.row_off = e * 2048 + 128; d.ilv = 1; }
;         else                  { r -= 2 * I_G; d.src = wd + eo; d.dst = WD; d.N = DM; d.K = FE; d.row_off = e * 2048; d.ilv = 0; }
;         const int nblk = d.N / 32; d.k0 = 64 * (r / nblk); d.n0 = 32 * (r % nblk); return d; };
;     ...
;         hb = (it + nw < it1);
;         if (hb) { db = decode(it + nw); cvt_load(db, vb, lane); }
;         if (!ha) break;
;     }
	v_bfe_u32 v67, v86, 16, 1
	v_add3_u32 v67, v86, v67, s43
	s_waitcnt lgkmcnt(2)
	v_bfe_u32 v79, v84, 16, 1
	ds_read2_b32 v[92:93], v73 offset0:148 offset1:156
	v_lshrrev_b32_e32 v67, 16, v67
	v_add3_u32 v79, v84, v79, s43
	ds_read2_b32 v[94:95], v73 offset0:181 offset1:189
	v_and_or_b32 v80, v79, s44, v67
	s_waitcnt lgkmcnt(3)
	v_bfe_u32 v67, v88, 16, 1
	v_add3_u32 v67, v88, v67, s43
	s_waitcnt lgkmcnt(2)
	v_bfe_u32 v79, v90, 16, 1
	ds_read2_b32 v[96:97], v73 offset0:214 offset1:222
	v_lshrrev_b32_e32 v67, 16, v67
	v_add3_u32 v79, v90, v79, s43
	ds_read2_b32 v[98:99], v73 offset0:247 offset1:255
	v_and_or_b32 v81, v79, s44, v67
	s_waitcnt lgkmcnt(3)
	v_bfe_u32 v67, v92, 16, 1
	v_add3_u32 v67, v92, v67, s43
	s_waitcnt lgkmcnt(2)
	v_bfe_u32 v79, v94, 16, 1
	v_lshrrev_b32_e32 v67, 16, v67
	v_add3_u32 v79, v94, v79, s43
	v_and_or_b32 v82, v79, s44, v67
	s_waitcnt lgkmcnt(1)
	v_bfe_u32 v67, v96, 16, 1
	v_add3_u32 v67, v96, v67, s43
	s_waitcnt lgkmcnt(0)
	v_bfe_u32 v79, v98, 16, 1
	v_lshrrev_b32_e32 v67, 16, v67
	v_add3_u32 v79, v98, v79, s43
	v_and_or_b32 v83, v79, s44, v67
	v_add_u32_e32 v67, s22, v71
	v_lshlrev_b32_e32 v79, 1, v67
	v_and_b32_e32 v84, 0x7f, v67
	v_and_or_b32 v79, v79, s45, v84
	v_cndmask_b32_e32 v67, v79, v67, vcc
	v_add_u32_e32 v67, s41, v67
	v_mad_u64_u32 v[100:101], s[16:17], v67, s40, 0
	v_ashrrev_i32_e32 v79, 31, v67
	v_mov_b32_e32 v84, v101
	v_mad_u64_u32 v[102:103], s[16:17], v79, s40, v[84:85]
	v_mov_b32_e32 v101, v102
	v_lshl_add_u64 v[100:101], v[100:101], 1, s[12:13]
	v_bfe_u32 v67, v87, 16, 1
	v_lshl_add_u64 v[100:101], v[100:101], 0, s[2:3]
	v_add3_u32 v67, v87, v67, s43
	v_bfe_u32 v79, v85, 16, 1
	v_lshl_add_u64 v[100:101], v[100:101], 0, v[68:69]
	v_lshrrev_b32_e32 v67, 16, v67
	v_add3_u32 v79, v85, v79, s43
	global_store_dwordx4 v[100:101], v[80:83], off nt
	s_nop 1
	v_and_or_b32 v80, v79, s44, v67
	v_bfe_u32 v67, v89, 16, 1
	v_add3_u32 v67, v89, v67, s43
	v_bfe_u32 v79, v91, 16, 1
	v_lshrrev_b32_e32 v67, 16, v67
	v_add3_u32 v79, v91, v79, s43
	v_and_or_b32 v81, v79, s44, v67
	v_bfe_u32 v67, v93, 16, 1
	v_add3_u32 v67, v93, v67, s43
	v_bfe_u32 v79, v95, 16, 1
	v_lshrrev_b32_e32 v67, 16, v67
	v_add3_u32 v79, v95, v79, s43
	v_and_or_b32 v82, v79, s44, v67
	v_bfe_u32 v67, v97, 16, 1
	v_add3_u32 v67, v97, v67, s43
	v_bfe_u32 v79, v99, 16, 1
	v_lshrrev_b32_e32 v67, 16, v67
	v_add3_u32 v79, v99, v79, s43
	v_and_or_b32 v83, v79, s44, v67
	v_add_u32_e32 v67, s22, v72
	v_lshlrev_b32_e32 v79, 1, v67
	v_and_b32_e32 v84, 0x7f, v67
	v_and_or_b32 v79, v79, s45, v84
	v_cndmask_b32_e32 v67, v79, v67, vcc
	v_add_u32_e32 v67, s41, v67
	v_mad_u64_u32 v[84:85], s[16:17], v67, s40, 0
	v_ashrrev_i32_e32 v79, 31, v67
	v_mov_b32_e32 v86, v85
	v_mad_u64_u32 v[86:87], s[16:17], v79, s40, v[86:87]
	v_mov_b32_e32 v85, v86
	v_lshl_add_u64 v[84:85], v[84:85], 1, s[12:13]
	v_lshl_add_u64 v[84:85], v[84:85], 0, s[2:3]
	v_lshl_add_u64 v[84:85], v[84:85], 0, v[68:69]
	global_store_dwordx4 v[84:85], v[80:83], off nt
	s_add_i32 s2, s28, s39
	s_addk_i32 s2, 0xebc0
	s_waitcnt lgkmcnt(0)
	s_cmp_lt_i32 s2, 0xc000
	s_cselect_b64 s[16:17], -1, 0
	s_cmp_gt_i32 s2, 0xbfff
	s_cbranch_scc1 .LBB0_449
	s_mul_hi_i32 s3, s2, 0x2aaaaaab
	s_lshr_b32 s9, s3, 31
	s_ashr_i32 s3, s3, 9
	s_add_i32 s12, s3, s9
	s_mul_i32 s3, s12, 0xc00
	s_ashr_i32 s13, s12, 31
	s_sub_i32 s11, s2, s3
	s_lshl_b64 s[20:21], s[12:13], 21
	s_lshl_b32 s26, s12, 11
	s_cmpk_gt_i32 s11, 0x3ff
	s_mov_b64 s[22:23], -1
	s_cbranch_scc0 .LBB0_467
	s_cmpk_gt_u32 s11, 0x7ff
	s_mov_b64 s[12:13], -1
	s_cbranch_scc0 .LBB0_465
	s_add_i32 s9, s11, 0xfffff800
	s_lshl_b64 s[2:3], s[20:21], 2
	s_add_u32 s2, s36, s2
	s_addc_u32 s3, s35, s3
	s_mov_b64 s[12:13], 0

; #define LAS __attribute__((address_space(3)))
; __device__ __forceinline__ unsigned pk2(float lo, float hi) { return f2bf(lo) | (f2bf(hi) << 16); }
;     __device__ __forceinline__ const float* x() const { return (const float*)ld(0); }
;     __device__ __forceinline__ const float* c() const { return (const float*)ld(1); }
; template <bool NT = true> __device__ __forceinline__ void cvt_store(const CvtItem& d, const f32x4 (&v)[8], LAS float* scr, int lane) {
;     const int rr = lane >> 3, c4 = (lane & 7) * 4;
; #pragma unroll
;     for (int q = 0; q < 8; ++q) { LAS float* t = scr + (8 * q + rr) * 33 + c4; t[0] = v[q].x; t[1] = v[q].y; t[2] = v[q].z; t[3] = v[q].w; }
;     asm volatile("s_waitcnt lgkmcnt(0)" ::: "memory");
;     const int c = lane & 7;
; #pragma unroll
;     for (int j = 0; j < 4; ++j) { const int n = (lane >> 3) + 8 * j; const LAS float* s = scr + (8 * c) * 33 + n;
;         u32x4 o; o.x = pk2(s[0 * 33], s[1 * 33]); o.y = pk2(s[2 * 33], s[3 * 33]); o.z = pk2(s[4 * 33], s[5 * 33]); o.w = pk2(s[6 * 33], s[7 * 33]);
;         const int ng = d.n0 + n, drow = d.row_off + (d.ilv ? ((ng >> 7) * 256 + (ng & 127)) : ng);
;         if (NT) __builtin_nontemporal_store(o, (u32x4*)(d.dst + (size_t)drow * d.K + d.k0 + 8 * c)); else *(u32x4*)(d.dst + (size_t)drow * d.K + d.k0 + 8 * c) = o; }
;     asm volatile("s_waitcnt lgkmcnt(0)" ::: "memory");
; }
; __device__ __forceinline__ void convert_moe_items(const Ctx& a, int layer, LAS unsigned char* lds, int it0, int it1, int widx, int nw, int wave, int lane) {
;     ...
;     for (;;) {
;         cvt_store(da, va, scr, lane);
;         it += 2 * nw; const bool ha = (it < it1);
;         if (ha) { da = decode(it); cvt_load(da, va, lane); }
.LBB0_678:
	s_cmp_lg_u64 s[18:19], 0
	s_cbranch_scc1 .Lcvt_p4c_t
	s_waitcnt vmcnt(0)
.Lcvt_p4c_t:
	v_add_u32_e32 v79, 0x420, v74
	v_add_u32_e32 v80, 0x428, v74
	v_add_u32_e32 v81, 0x840, v74
	v_add_u32_e32 v82, 0x848, v74
	v_add_u32_e32 v83, 0xc60, v74
	v_add_u32_e32 v84, 0xc68, v74
	v_add_u32_e32 v85, 0x1080, v74
	v_add_u32_e32 v86, 0x1088, v74
	v_add_u32_e32 v87, 0x14a0, v74
	v_add_u32_e32 v88, 0x14a8, v74
	v_add_u32_e32 v89, 0x18c0, v74
	v_add_u32_e32 v90, 0x18c8, v74
	v_add_u32_e32 v91, 0x1ce0, v74
	v_add_u32_e32 v92, 0x1ce8, v74
	s_waitcnt vmcnt(15)
	ds_write2_b32 v74, v2, v3 offset1:1
	ds_write2_b32 v74, v4, v5 offset0:2 offset1:3
	s_waitcnt vmcnt(14)
	ds_write2_b32 v79, v6, v7 offset1:1
	ds_write2_b32 v80, v8, v9 offset1:1
	s_waitcnt vmcnt(13)
	ds_write2_b32 v81, v10, v11 offset1:1
	ds_write2_b32 v82, v12, v13 offset1:1
	s_waitcnt vmcnt(12)
	ds_write2_b32 v83, v14, v15 offset1:1
	ds_write2_b32 v84, v16, v17 offset1:1
	s_waitcnt vmcnt(11)
	ds_write2_b32 v85, v18, v19 offset1:1
	ds_write2_b32 v86, v20, v21 offset1:1
	s_waitcnt vmcnt(10)
	ds_write2_b32 v87, v22, v23 offset1:1
	ds_write2_b32 v88, v24, v25 offset1:1
	s_waitcnt vmcnt(9)
	ds_write2_b32 v89, v26, v27 offset1:1
	ds_write2_b32 v90, v28, v29 offset1:1
	s_waitcnt vmcnt(8)
	ds_write2_b32 v91, v30, v31 offset1:1
	ds_write2_b32 v92, v32, v33 offset1:1
	s_waitcnt lgkmcnt(0)
	ds_read2_b32 v[98:99], v73 offset1:8
	ds_read2_b32 v[100:101], v73 offset0:33 offset1:41
	ds_read2_b32 v[102:103], v73 offset0:66 offset1:74
	ds_read2_b32 v[104:105], v73 offset0:99 offset1:107
	ds_read2_b32 v[106:107], v73 offset0:132 offset1:140
	s_waitcnt lgkmcnt(4)
	v_bfe_u32 v67, v98, 16, 1
	v_add3_u32 v67, v98, v67, s51
	s_waitcnt lgkmcnt(3)
	v_bfe_u32 v93, v100, 16, 1
	v_lshrrev_b32_e32 v67, 16, v67
	v_add3_u32 v93, v100, v93, s51
	ds_read2_b32 v[108:109], v73 offset0:165 offset1:173
	v_and_or_b32 v94, v93, s52, v67
	s_waitcnt lgkmcnt(3)
	v_bfe_u32 v67, v102, 16, 1
	v_add3_u32 v67, v102, v67, s51
	s_waitcnt lgkmcnt(2)
	v_bfe_u32 v93, v104, 16, 1
	ds_read2_b32 v[110:111], v73 offset0:198 offset1:206
	v_lshrrev_b32_e32 v67, 16, v67
	v_add3_u32 v93, v104, v93, s51
	ds_read2_b32 v[112:113], v73 offset0:231 offset1:239
	v_and_or_b32 v95, v93, s52, v67
	s_waitcnt lgkmcnt(3)
	v_bfe_u32 v67, v106, 16, 1
	v_add3_u32 v67, v106, v67, s51
	s_waitcnt lgkmcnt(2)
	v_bfe_u32 v93, v108, 16, 1
	v_lshrrev_b32_e32 v67, 16, v67
	v_add3_u32 v93, v108, v93, s51
	v_and_or_b32 v96, v93, s52, v67
	s_waitcnt lgkmcnt(1)
	v_bfe_u32 v67, v110, 16, 1
	v_add3_u32 v67, v110, v67, s51
	s_waitcnt lgkmcnt(0)
	v_bfe_u32 v93, v112, 16, 1
	s_cmp_eq_u32 s29, 0
	v_lshrrev_b32_e32 v67, 16, v67
	v_add3_u32 v93, v112, v93, s51
	s_cselect_b64 vcc, -1, 0
	s_lshl_b32 s2, s14, 1
	v_and_or_b32 v97, v93, s52, v67
	s_and_b32 s15, s2, 0xffffff00
	v_bitop3_b32 v93, s14, v75, v1 bitop3:0xc8
	v_or_b32_e32 v67, s14, v1
	v_or_b32_e32 v93, s15, v93
	v_cndmask_b32_e32 v67, v93, v67, vcc
	v_add_u32_e32 v67, s40, v67
	v_mad_u64_u32 v[114:115], s[2:3], v67, s39, 0
	v_ashrrev_i32_e32 v93, 31, v67
	v_mov_b32_e32 v98, v115
	v_mad_u64_u32 v[116:117], s[2:3], v93, s39, v[98:99]
	v_mov_b32_e32 v115, v116
	s_ashr_i32 s13, s12, 31
	v_lshl_add_u64 v[114:115], v[114:115], 1, s[10:11]
	s_lshl_b64 s[2:3], s[12:13], 1
	v_bfe_u32 v67, v99, 16, 1
	v_lshl_add_u64 v[114:115], v[114:115], 0, s[2:3]
	v_add3_u32 v67, v99, v67, s51
	v_bfe_u32 v93, v101, 16, 1
	v_lshl_add_u64 v[114:115], v[114:115], 0, v[68:69]
	v_lshrrev_b32_e32 v67, 16, v67
	v_add3_u32 v93, v101, v93, s51
	global_store_dwordx4 v[114:115], v[94:97], off nt
	s_add_i32 s54, s41, s49
	s_cmp_gt_i32 s54, 0xa7ff
	v_and_or_b32 v94, v93, s52, v67
	v_bfe_u32 v67, v103, 16, 1
	v_add3_u32 v67, v103, v67, s51
	v_bfe_u32 v93, v105, 16, 1
	v_lshrrev_b32_e32 v67, 16, v67
	v_add3_u32 v93, v105, v93, s51
	v_and_or_b32 v95, v93, s52, v67
	v_bfe_u32 v67, v107, 16, 1
	v_add3_u32 v67, v107, v67, s51
	v_bfe_u32 v93, v109, 16, 1
	v_lshrrev_b32_e32 v67, 16, v67
	v_add3_u32 v93, v109, v93, s51
	v_and_or_b32 v96, v93, s52, v67
	v_bfe_u32 v67, v111, 16, 1
	v_add3_u32 v67, v111, v67, s51
	v_bfe_u32 v93, v113, 16, 1
	v_lshrrev_b32_e32 v67, 16, v67
	v_add3_u32 v93, v113, v93, s51
	v_and_or_b32 v97, v93, s52, v67
	v_bitop3_b32 v93, s14, v76, v70 bitop3:0xc8
	v_or_b32_e32 v67, s14, v70
	v_or_b32_e32 v93, s15, v93
	v_cndmask_b32_e32 v67, v93, v67, vcc
	v_add_u32_e32 v67, s40, v67
	v_mad_u64_u32 v[98:99], s[26:27], v67, s39, 0
	v_ashrrev_i32_e32 v93, 31, v67
	v_mov_b32_e32 v100, v99
	v_mad_u64_u32 v[100:101], s[26:27], v93, s39, v[100:101]
	v_mov_b32_e32 v99, v100
	v_lshl_add_u64 v[98:99], v[98:99], 1, s[10:11]
	v_lshl_add_u64 v[98:99], v[98:99], 0, s[2:3]
	ds_read2_b32 v[100:101], v73 offset0:16 offset1:24
	v_lshl_add_u64 v[98:99], v[98:99], 0, v[68:69]
	global_store_dwordx4 v[98:99], v[94:97], off nt
	ds_read2_b32 v[98:99], v73 offset0:49 offset1:57
	ds_read2_b32 v[102:103], v73 offset0:82 offset1:90
	ds_read2_b32 v[104:105], v73 offset0:115 offset1:123
	s_waitcnt lgkmcnt(3)
; #define LAS __attribute__((address_space(3)))
; __device__ __forceinline__ unsigned pk2(float lo, float hi) { return f2bf(lo) | (f2bf(hi) << 16); }
;     __device__ __forceinline__ const float* x() const { return (const float*)ld(0); }
;     __device__ __forceinline__ const float* c() const { return (const float*)ld(1); }
; template <bool NT = true> __device__ __forceinline__ void cvt_store(const CvtItem& d, const f32x4 (&v)[8], LAS float* scr, int lane) {
;     ...
;     for (int j = 0; j < 4; ++j) { const int n = (lane >> 3) + 8 * j; const LAS float* s = scr + (8 * c) * 33 + n;
;         u32x4 o; o.x = pk2(s[0 * 33], s[1 * 33]); o.y = pk2(s[2 * 33], s[3 * 33]); o.z = pk2(s[4 * 33], s[5 * 33]); o.w = pk2(s[6 * 33], s[7 * 33]);
;         const int ng = d.n0 + n, drow = d.row_off + (d.ilv ? ((ng >> 7) * 256 + (ng & 127)) : ng);
;         if (NT) __builtin_nontemporal_store(o, (u32x4*)(d.dst + (size_t)drow * d.K + d.k0 + 8 * c)); else *(u32x4*)(d.dst + (size_t)drow * d.K + d.k0 + 8 * c) = o; }
;     asm volatile("s_waitcnt lgkmcnt(0)" ::: "memory");
; __device__ __forceinline__ void convert_moe_items(const Ctx& a, int layer, LAS unsigned char* lds, int it0, int it1, int widx, int nw, int wave, int lane) {
;     ...
;     auto decode = [&](int it) { CvtItem d; const int e = it / PER_E; int r = it % PER_E; const size_t eo = ((size_t)layer * NE + e) * (size_t)DM * FE;
;         if (r < I_G)          { d.src = wg + eo; d.dst = WGU; d.N = FE; d.K = DM; d.row_off = e * 2048; d.ilv = 1; }
;         else if (r < 2 * I_G) { r -= I_G; d.src = wu + eo; d.dst = WGU; d.N = FE; d.K = DM; d.row_off = e * 2048 + 128; d.ilv = 1; }
;         else                  { r -= 2 * I_G; d.src = wd + eo; d.dst = WD; d.N = DM; d.K = FE; d.row_off = e * 2048; d.ilv = 0; }
;         const int nblk = d.N / 32; d.k0 = 64 * (r / nblk); d.n0 = 32 * (r % nblk); return d; };
	v_bfe_u32 v67, v100, 16, 1
	v_add3_u32 v67, v100, v67, s51
	s_waitcnt lgkmcnt(2)
	v_bfe_u32 v93, v98, 16, 1
	ds_read2_b32 v[106:107], v73 offset0:148 offset1:156
	v_lshrrev_b32_e32 v67, 16, v67
	v_add3_u32 v93, v98, v93, s51
	ds_read2_b32 v[108:109], v73 offset0:181 offset1:189
	v_and_or_b32 v94, v93, s52, v67
	s_waitcnt lgkmcnt(3)
	v_bfe_u32 v67, v102, 16, 1
	v_add3_u32 v67, v102, v67, s51
	s_waitcnt lgkmcnt(2)
	v_bfe_u32 v93, v104, 16, 1
	ds_read2_b32 v[110:111], v73 offset0:214 offset1:222
	v_lshrrev_b32_e32 v67, 16, v67
	v_add3_u32 v93, v104, v93, s51
	ds_read2_b32 v[112:113], v73 offset0:247 offset1:255
	v_and_or_b32 v95, v93, s52, v67
	s_waitcnt lgkmcnt(3)
	v_bfe_u32 v67, v106, 16, 1
	v_add3_u32 v67, v106, v67, s51
	s_waitcnt lgkmcnt(2)
	v_bfe_u32 v93, v108, 16, 1
	v_lshrrev_b32_e32 v67, 16, v67
	v_add3_u32 v93, v108, v93, s51
	v_and_or_b32 v96, v93, s52, v67
	s_waitcnt lgkmcnt(1)
	v_bfe_u32 v67, v110, 16, 1
	v_add3_u32 v67, v110, v67, s51
	s_waitcnt lgkmcnt(0)
	v_bfe_u32 v93, v112, 16, 1
	v_lshrrev_b32_e32 v67, 16, v67
	v_add3_u32 v93, v112, v93, s51
	v_and_or_b32 v97, v93, s52, v67
	v_bitop3_b32 v93, s14, v77, v71 bitop3:0xc8
	v_or_b32_e32 v67, s14, v71
	v_or_b32_e32 v93, s15, v93
	v_cndmask_b32_e32 v67, v93, v67, vcc
	v_add_u32_e32 v67, s40, v67
	v_mad_u64_u32 v[114:115], s[26:27], v67, s39, 0
	v_ashrrev_i32_e32 v93, 31, v67
	v_mov_b32_e32 v98, v115
	v_mad_u64_u32 v[116:117], s[26:27], v93, s39, v[98:99]
	v_mov_b32_e32 v115, v116
	v_lshl_add_u64 v[114:115], v[114:115], 1, s[10:11]
	v_bfe_u32 v67, v101, 16, 1
	v_lshl_add_u64 v[114:115], v[114:115], 0, s[2:3]
	v_add3_u32 v67, v101, v67, s51
	v_bfe_u32 v93, v99, 16, 1
	v_lshl_add_u64 v[114:115], v[114:115], 0, v[68:69]
	v_lshrrev_b32_e32 v67, 16, v67
	v_add3_u32 v93, v99, v93, s51
	global_store_dwordx4 v[114:115], v[94:97], off nt
	s_nop 1
	v_and_or_b32 v94, v93, s52, v67
	v_bfe_u32 v67, v103, 16, 1
	v_add3_u32 v67, v103, v67, s51
	v_bfe_u32 v93, v105, 16, 1
	v_lshrrev_b32_e32 v67, 16, v67
	v_add3_u32 v93, v105, v93, s51
	v_and_or_b32 v95, v93, s52, v67
	v_bfe_u32 v67, v107, 16, 1
	v_add3_u32 v67, v107, v67, s51
	v_bfe_u32 v93, v109, 16, 1
	v_lshrrev_b32_e32 v67, 16, v67
	v_add3_u32 v93, v109, v93, s51
	v_and_or_b32 v96, v93, s52, v67
	v_bfe_u32 v67, v111, 16, 1
	v_add3_u32 v67, v111, v67, s51
	v_bfe_u32 v93, v113, 16, 1
	v_lshrrev_b32_e32 v67, 16, v67
	v_add3_u32 v93, v113, v93, s51
	v_and_or_b32 v97, v93, s52, v67
	v_bitop3_b32 v93, s14, v78, v72 bitop3:0xc8
	v_or_b32_e32 v67, s14, v72
	v_or_b32_e32 v93, s15, v93
	v_cndmask_b32_e32 v67, v93, v67, vcc
	v_add_u32_e32 v67, s40, v67
	v_mad_u64_u32 v[98:99], s[26:27], v67, s39, 0
	v_ashrrev_i32_e32 v93, 31, v67
	v_mov_b32_e32 v100, v99
	v_mad_u64_u32 v[100:101], s[26:27], v93, s39, v[100:101]
	v_mov_b32_e32 v99, v100
	v_lshl_add_u64 v[98:99], v[98:99], 1, s[10:11]
	v_lshl_add_u64 v[98:99], v[98:99], 0, s[2:3]
	v_lshl_add_u64 v[98:99], v[98:99], 0, v[68:69]
	global_store_dwordx4 v[98:99], v[94:97], off nt
	s_waitcnt lgkmcnt(0)
	s_cselect_b64 s[26:27], -1, 0
	s_and_b64 vcc, exec, s[26:27]
	s_cbranch_vccnz .LBB0_687
	s_mul_hi_i32 s2, s54, 0x2aaaaaab
	s_lshr_b32 s3, s2, 31
	s_ashr_i32 s2, s2, 9
	s_add_i32 s28, s2, s3
	s_mul_i32 s2, s28, 0xfffff400
	s_ashr_i32 s29, s28, 31
	s_add_i32 s23, s54, s2
	s_lshl_b64 s[2:3], s[28:29], 21
	s_add_u32 s12, s2, 0x2000000
	s_addc_u32 s13, s3, 0
	s_lshl_b32 s55, s28, 11
	s_cmpk_gt_i32 s23, 0x3ff
	s_mov_b64 s[14:15], -1
	s_cbranch_scc0 .LBB0_684
	s_mul_i32 s2, s28, 0xc00
	s_sub_i32 s14, s54, s2
	s_cmpk_gt_u32 s23, 0x7ff
	s_mov_b64 s[10:11], -1
	s_cbranch_scc0 .LBB0_682
	s_add_i32 s25, s14, 0xfffff800
	s_lshl_b64 s[2:3], s[12:13], 2
	s_add_u32 s2, s38, s2
	s_addc_u32 s3, s37, s3
	s_mov_b64 s[10:11], 0

; #define LAS __attribute__((address_space(3)))
; __device__ __forceinline__ unsigned pk2(float lo, float hi) { return f2bf(lo) | (f2bf(hi) << 16); }
;     __device__ __forceinline__ const float* x() const { return (const float*)ld(0); }
;     __device__ __forceinline__ const float* c() const { return (const float*)ld(1); }
; template <bool NT = true> __device__ __forceinline__ void cvt_store(const CvtItem& d, const f32x4 (&v)[8], LAS float* scr, int lane) {
;     const int rr = lane >> 3, c4 = (lane & 7) * 4;
; #pragma unroll
;     for (int q = 0; q < 8; ++q) { LAS float* t = scr + (8 * q + rr) * 33 + c4; t[0] = v[q].x; t[1] = v[q].y; t[2] = v[q].z; t[3] = v[q].w; }
;     asm volatile("s_waitcnt lgkmcnt(0)" ::: "memory");
;     const int c = lane & 7;
; #pragma unroll
;     for (int j = 0; j < 4; ++j) { const int n = (lane >> 3) + 8 * j; const LAS float* s = scr + (8 * c) * 33 + n;
;         u32x4 o; o.x = pk2(s[0 * 33], s[1 * 33]); o.y = pk2(s[2 * 33], s[3 * 33]); o.z = pk2(s[4 * 33], s[5 * 33]); o.w = pk2(s[6 * 33], s[7 * 33]);
;         const int ng = d.n0 + n, drow = d.row_off + (d.ilv ? ((ng >> 7) * 256 + (ng & 127)) : ng);
;         if (NT) __builtin_nontemporal_store(o, (u32x4*)(d.dst + (size_t)drow * d.K + d.k0 + 8 * c)); else *(u32x4*)(d.dst + (size_t)drow * d.K + d.k0 + 8 * c) = o; }
;     asm volatile("s_waitcnt lgkmcnt(0)" ::: "memory");
; }
; __device__ __forceinline__ void convert_moe_items(const Ctx& a, int layer, LAS unsigned char* lds, int it0, int it1, int widx, int nw, int wave, int lane) {
;     ...
;         cvt_store(db, vb, scr, lane);
;         hb = (it + nw < it1);
;         if (hb) { db = decode(it + nw); cvt_load(db, vb, lane); }
.LBB0_688:
	s_cmp_lg_u64 s[26:27], 0
	s_cbranch_scc0 .Lcvt_p4c_m
	s_waitcnt vmcnt(0)
.Lcvt_p4c_m:
	s_waitcnt vmcnt(12)
	ds_write2_b32 v74, v34, v35 offset1:1
	ds_write2_b32 v74, v36, v37 offset0:2 offset1:3
	ds_write2_b32 v79, v38, v39 offset1:1
	ds_write2_b32 v80, v40, v41 offset1:1
	ds_write2_b32 v81, v42, v43 offset1:1
	ds_write2_b32 v82, v44, v45 offset1:1
	ds_write2_b32 v83, v46, v47 offset1:1
	ds_write2_b32 v84, v48, v49 offset1:1
	ds_write2_b32 v85, v50, v51 offset1:1
	ds_write2_b32 v86, v52, v53 offset1:1
	ds_write2_b32 v87, v54, v55 offset1:1
	ds_write2_b32 v88, v56, v57 offset1:1
	ds_write2_b32 v89, v58, v59 offset1:1
	ds_write2_b32 v90, v60, v61 offset1:1
	ds_write2_b32 v91, v62, v63 offset1:1
	ds_write2_b32 v92, v64, v65 offset1:1
	s_waitcnt lgkmcnt(0)
	ds_read2_b32 v[84:85], v73 offset1:8
	ds_read2_b32 v[86:87], v73 offset0:33 offset1:41
	ds_read2_b32 v[88:89], v73 offset0:66 offset1:74
	ds_read2_b32 v[90:91], v73 offset0:99 offset1:107
	ds_read2_b32 v[92:93], v73 offset0:132 offset1:140
	s_waitcnt lgkmcnt(4)
	v_bfe_u32 v67, v84, 16, 1
	v_add3_u32 v67, v84, v67, s51
	s_waitcnt lgkmcnt(3)
	v_bfe_u32 v79, v86, 16, 1
	v_lshrrev_b32_e32 v67, 16, v67
	v_add3_u32 v79, v86, v79, s51
	ds_read2_b32 v[94:95], v73 offset0:165 offset1:173
	v_and_or_b32 v80, v79, s52, v67
	s_waitcnt lgkmcnt(3)
	v_bfe_u32 v67, v88, 16, 1
	v_add3_u32 v67, v88, v67, s51
	s_waitcnt lgkmcnt(2)
	v_bfe_u32 v79, v90, 16, 1
	ds_read2_b32 v[96:97], v73 offset0:198 offset1:206
	v_lshrrev_b32_e32 v67, 16, v67
	v_add3_u32 v79, v90, v79, s51
	ds_read2_b32 v[98:99], v73 offset0:231 offset1:239
	v_and_or_b32 v81, v79, s52, v67
	s_waitcnt lgkmcnt(3)
	v_bfe_u32 v67, v92, 16, 1
	v_add3_u32 v67, v92, v67, s51
	s_waitcnt lgkmcnt(2)
	v_bfe_u32 v79, v94, 16, 1
	v_lshrrev_b32_e32 v67, 16, v67
	v_add3_u32 v79, v94, v79, s51
	v_and_or_b32 v82, v79, s52, v67
	s_waitcnt lgkmcnt(1)
	v_bfe_u32 v67, v96, 16, 1
	v_add3_u32 v67, v96, v67, s51
	s_waitcnt lgkmcnt(0)
	v_bfe_u32 v79, v98, 16, 1
	v_lshrrev_b32_e32 v67, 16, v67
	v_add3_u32 v79, v98, v79, s51
	v_and_or_b32 v83, v79, s52, v67
	v_add_u32_e32 v67, s24, v1
	s_cmp_eq_u32 s46, 0
	v_lshlrev_b32_e32 v79, 1, v67
	v_and_b32_e32 v84, 0x7f, v67
	v_and_or_b32 v79, v79, s53, v84
	s_cselect_b64 vcc, -1, 0
	v_cndmask_b32_e32 v67, v79, v67, vcc
	v_add_u32_e32 v67, s48, v67
	v_mad_u64_u32 v[100:101], s[2:3], v67, s47, 0
	v_ashrrev_i32_e32 v79, 31, v67
	v_mov_b32_e32 v84, v101
	v_mad_u64_u32 v[102:103], s[2:3], v79, s47, v[84:85]
	v_mov_b32_e32 v101, v102
	s_ashr_i32 s23, s22, 31
	v_lshl_add_u64 v[100:101], v[100:101], 1, s[16:17]
	s_lshl_b64 s[2:3], s[22:23], 1
	v_bfe_u32 v67, v85, 16, 1
	v_lshl_add_u64 v[100:101], v[100:101], 0, s[2:3]
	v_add3_u32 v67, v85, v67, s51
	v_bfe_u32 v79, v87, 16, 1
	v_lshl_add_u64 v[100:101], v[100:101], 0, v[68:69]
	v_lshrrev_b32_e32 v67, 16, v67
	v_add3_u32 v79, v87, v79, s51
	global_store_dwordx4 v[100:101], v[80:83], off nt
	s_nop 1
	v_and_or_b32 v80, v79, s52, v67
	v_bfe_u32 v67, v89, 16, 1
	v_add3_u32 v67, v89, v67, s51
	v_bfe_u32 v79, v91, 16, 1
	v_lshrrev_b32_e32 v67, 16, v67
	v_add3_u32 v79, v91, v79, s51
	v_and_or_b32 v81, v79, s52, v67
	v_bfe_u32 v67, v93, 16, 1
	v_add3_u32 v67, v93, v67, s51
	v_bfe_u32 v79, v95, 16, 1
	v_lshrrev_b32_e32 v67, 16, v67
	v_add3_u32 v79, v95, v79, s51
	v_and_or_b32 v82, v79, s52, v67
	v_bfe_u32 v67, v97, 16, 1
	v_add3_u32 v67, v97, v67, s51
	v_bfe_u32 v79, v99, 16, 1
	v_lshrrev_b32_e32 v67, 16, v67
	v_add3_u32 v79, v99, v79, s51
	v_and_or_b32 v83, v79, s52, v67
	v_add_u32_e32 v67, s24, v70
	v_lshlrev_b32_e32 v79, 1, v67
	v_and_b32_e32 v84, 0x7f, v67
	v_and_or_b32 v79, v79, s53, v84
	v_cndmask_b32_e32 v67, v79, v67, vcc
	v_add_u32_e32 v67, s48, v67
	v_mad_u64_u32 v[84:85], s[18:19], v67, s47, 0
	v_ashrrev_i32_e32 v79, 31, v67
	v_mov_b32_e32 v86, v85
	v_mad_u64_u32 v[86:87], s[18:19], v79, s47, v[86:87]
	v_mov_b32_e32 v85, v86
	v_lshl_add_u64 v[84:85], v[84:85], 1, s[16:17]
	v_lshl_add_u64 v[84:85], v[84:85], 0, s[2:3]
	ds_read2_b32 v[86:87], v73 offset0:16 offset1:24
	v_lshl_add_u64 v[84:85], v[84:85], 0, v[68:69]
	global_store_dwordx4 v[84:85], v[80:83], off nt
	ds_read2_b32 v[84:85], v73 offset0:49 offset1:57
	ds_read2_b32 v[88:89], v73 offset0:82 offset1:90
	ds_read2_b32 v[90:91], v73 offset0:115 offset1:123
	s_waitcnt lgkmcnt(3)
; #define LAS __attribute__((address_space(3)))
; __device__ __forceinline__ unsigned pk2(float lo, float hi) { return f2bf(lo) | (f2bf(hi) << 16); }
;     __device__ __forceinline__ const float* x() const { return (const float*)ld(0); }
;     __device__ __forceinline__ const float* c() const { return (const float*)ld(1); }
; template <bool NT = true> __device__ __forceinline__ void cvt_store(const CvtItem& d, const f32x4 (&v)[8], LAS float* scr, int lane) {
;     ...
;     for (int j = 0; j < 4; ++j) { const int n = (lane >> 3) + 8 * j; const LAS float* s = scr + (8 * c) * 33 + n;
;         u32x4 o; o.x = pk2(s[0 * 33], s[1 * 33]); o.y = pk2(s[2 * 33], s[3 * 33]); o.z = pk2(s[4 * 33], s[5 * 33]); o.w = pk2(s[6 * 33], s[7 * 33]);
;         const int ng = d.n0 + n, drow = d.row_off + (d.ilv ? ((ng >> 7) * 256 + (ng & 127)) : ng);
;         if (NT) __builtin_nontemporal_store(o, (u32x4*)(d.dst + (size_t)drow * d.K + d.k0 + 8 * c)); else *(u32x4*)(d.dst + (size_t)drow * d.K + d.k0 + 8 * c) = o; }
;     asm volatile("s_waitcnt lgkmcnt(0)" ::: "memory");
; __device__ __forceinline__ void convert_moe_items(const Ctx& a, int layer, LAS unsigned char* lds, int it0, int it1, int widx, int nw, int wave, int lane) {
;     ...
;     auto decode = [&](int it) { CvtItem d; const int e = it / PER_E; int r = it % PER_E; const size_t eo = ((size_t)layer * NE + e) * (size_t)DM * FE;
;         if (r < I_G)          { d.src = wg + eo; d.dst = WGU; d.N = FE; d.K = DM; d.row_off = e * 2048; d.ilv = 1; }
;         else if (r < 2 * I_G) { r -= I_G; d.src = wu + eo; d.dst = WGU; d.N = FE; d.K = DM; d.row_off = e * 2048 + 128; d.ilv = 1; }
;         else                  { r -= 2 * I_G; d.src = wd + eo; d.dst = WD; d.N = DM; d.K = FE; d.row_off = e * 2048; d.ilv = 0; }
;         const int nblk = d.N / 32; d.k0 = 64 * (r / nblk); d.n0 = 32 * (r % nblk); return d; };
;     ...
;         hb = (it + nw < it1);
;         if (hb) { db = decode(it + nw); cvt_load(db, vb, lane); }
;         if (!ha) break;
;     }
	v_bfe_u32 v67, v86, 16, 1
	v_add3_u32 v67, v86, v67, s51
	s_waitcnt lgkmcnt(2)
	v_bfe_u32 v79, v84, 16, 1
	ds_read2_b32 v[92:93], v73 offset0:148 offset1:156
	v_lshrrev_b32_e32 v67, 16, v67
	v_add3_u32 v79, v84, v79, s51
	ds_read2_b32 v[94:95], v73 offset0:181 offset1:189
	v_and_or_b32 v80, v79, s52, v67
	s_waitcnt lgkmcnt(3)
	v_bfe_u32 v67, v88, 16, 1
	v_add3_u32 v67, v88, v67, s51
	s_waitcnt lgkmcnt(2)
	v_bfe_u32 v79, v90, 16, 1
	ds_read2_b32 v[96:97], v73 offset0:214 offset1:222
	v_lshrrev_b32_e32 v67, 16, v67
	v_add3_u32 v79, v90, v79, s51
	ds_read2_b32 v[98:99], v73 offset0:247 offset1:255
	v_and_or_b32 v81, v79, s52, v67
	s_waitcnt lgkmcnt(3)
	v_bfe_u32 v67, v92, 16, 1
	v_add3_u32 v67, v92, v67, s51
	s_waitcnt lgkmcnt(2)
	v_bfe_u32 v79, v94, 16, 1
	v_lshrrev_b32_e32 v67, 16, v67
	v_add3_u32 v79, v94, v79, s51
	v_and_or_b32 v82, v79, s52, v67
	s_waitcnt lgkmcnt(1)
	v_bfe_u32 v67, v96, 16, 1
	v_add3_u32 v67, v96, v67, s51
	s_waitcnt lgkmcnt(0)
	v_bfe_u32 v79, v98, 16, 1
	v_lshrrev_b32_e32 v67, 16, v67
	v_add3_u32 v79, v98, v79, s51
	v_and_or_b32 v83, v79, s52, v67
	v_add_u32_e32 v67, s24, v71
	v_lshlrev_b32_e32 v79, 1, v67
	v_and_b32_e32 v84, 0x7f, v67
	v_and_or_b32 v79, v79, s53, v84
	v_cndmask_b32_e32 v67, v79, v67, vcc
	v_add_u32_e32 v67, s48, v67
	v_mad_u64_u32 v[100:101], s[18:19], v67, s47, 0
	v_ashrrev_i32_e32 v79, 31, v67
	v_mov_b32_e32 v84, v101
	v_mad_u64_u32 v[102:103], s[18:19], v79, s47, v[84:85]
	v_mov_b32_e32 v101, v102
	v_lshl_add_u64 v[100:101], v[100:101], 1, s[16:17]
	v_bfe_u32 v67, v87, 16, 1
	v_lshl_add_u64 v[100:101], v[100:101], 0, s[2:3]
	v_add3_u32 v67, v87, v67, s51
	v_bfe_u32 v79, v85, 16, 1
	v_lshl_add_u64 v[100:101], v[100:101], 0, v[68:69]
	v_lshrrev_b32_e32 v67, 16, v67
	v_add3_u32 v79, v85, v79, s51
	global_store_dwordx4 v[100:101], v[80:83], off nt
	s_nop 1
	v_and_or_b32 v80, v79, s52, v67
	v_bfe_u32 v67, v89, 16, 1
	v_add3_u32 v67, v89, v67, s51
	v_bfe_u32 v79, v91, 16, 1
	v_lshrrev_b32_e32 v67, 16, v67
	v_add3_u32 v79, v91, v79, s51
	v_and_or_b32 v81, v79, s52, v67
	v_bfe_u32 v67, v93, 16, 1
	v_add3_u32 v67, v93, v67, s51
	v_bfe_u32 v79, v95, 16, 1
	v_lshrrev_b32_e32 v67, 16, v67
	v_add3_u32 v79, v95, v79, s51
	v_and_or_b32 v82, v79, s52, v67
	v_bfe_u32 v67, v97, 16, 1
	v_add3_u32 v67, v97, v67, s51
	v_bfe_u32 v79, v99, 16, 1
	v_lshrrev_b32_e32 v67, 16, v67
	v_add3_u32 v79, v99, v79, s51
	v_and_or_b32 v83, v79, s52, v67
	v_add_u32_e32 v67, s24, v72
	v_lshlrev_b32_e32 v79, 1, v67
	v_and_b32_e32 v84, 0x7f, v67
	v_and_or_b32 v79, v79, s53, v84
	v_cndmask_b32_e32 v67, v79, v67, vcc
	v_add_u32_e32 v67, s48, v67
	v_mad_u64_u32 v[84:85], s[18:19], v67, s47, 0
	v_ashrrev_i32_e32 v79, 31, v67
	v_mov_b32_e32 v86, v85
	v_mad_u64_u32 v[86:87], s[18:19], v79, s47, v[86:87]
	v_mov_b32_e32 v85, v86
	v_lshl_add_u64 v[84:85], v[84:85], 1, s[16:17]
	v_lshl_add_u64 v[84:85], v[84:85], 0, s[2:3]
	v_lshl_add_u64 v[84:85], v[84:85], 0, v[68:69]
	global_store_dwordx4 v[84:85], v[80:83], off nt
	s_add_i32 s2, s50, s41
	s_waitcnt lgkmcnt(0)
	s_cmp_lt_i32 s2, 0xa800
	s_cselect_b64 s[18:19], -1, 0
	s_cmp_gt_i32 s2, 0xa7ff
	s_cbranch_scc1 .LBB0_676
	s_mul_hi_i32 s3, s2, 0x2aaaaaab
	s_lshr_b32 s13, s3, 31
	s_ashr_i32 s3, s3, 9
	s_add_i32 s16, s3, s13
	s_mul_i32 s3, s16, 0xc00
	s_ashr_i32 s17, s16, 31
	s_sub_i32 s15, s2, s3
	s_lshl_b64 s[2:3], s[16:17], 21
	s_add_u32 s22, s2, 0x2000000
	s_addc_u32 s23, s3, 0
	s_lshl_b32 s28, s16, 11
	s_cmpk_gt_i32 s15, 0x3ff
	s_mov_b64 s[24:25], -1
	s_cbranch_scc0 .LBB0_694
	s_cmpk_gt_u32 s15, 0x7ff
	s_mov_b64 s[16:17], -1
	s_cbranch_scc0 .LBB0_692
	s_add_i32 s13, s15, 0xfffff800
	s_lshl_b64 s[2:3], s[22:23], 2
	s_add_u32 s2, s38, s2
	s_addc_u32 s3, s37, s3
	s_mov_b64 s[16:17], 0

; #define LAS __attribute__((address_space(3)))
; __device__ __forceinline__ unsigned pk2(float lo, float hi) { return f2bf(lo) | (f2bf(hi) << 16); }
;     __device__ __forceinline__ const float* x() const { return (const float*)ld(0); }
;     __device__ __forceinline__ const float* c() const { return (const float*)ld(1); }
; template <bool NT = true> __device__ __forceinline__ void cvt_store(const CvtItem& d, const f32x4 (&v)[8], LAS float* scr, int lane) {
;     const int rr = lane >> 3, c4 = (lane & 7) * 4;
; #pragma unroll
;     for (int q = 0; q < 8; ++q) { LAS float* t = scr + (8 * q + rr) * 33 + c4; t[0] = v[q].x; t[1] = v[q].y; t[2] = v[q].z; t[3] = v[q].w; }
;     asm volatile("s_waitcnt lgkmcnt(0)" ::: "memory");
;     const int c = lane & 7;
; #pragma unroll
;     for (int j = 0; j < 4; ++j) { const int n = (lane >> 3) + 8 * j; const LAS float* s = scr + (8 * c) * 33 + n;
;         u32x4 o; o.x = pk2(s[0 * 33], s[1 * 33]); o.y = pk2(s[2 * 33], s[3 * 33]); o.z = pk2(s[4 * 33], s[5 * 33]); o.w = pk2(s[6 * 33], s[7 * 33]);
;         const int ng = d.n0 + n, drow = d.row_off + (d.ilv ? ((ng >> 7) * 256 + (ng & 127)) : ng);
;         if (NT) __builtin_nontemporal_store(o, (u32x4*)(d.dst + (size_t)drow * d.K + d.k0 + 8 * c)); else *(u32x4*)(d.dst + (size_t)drow * d.K + d.k0 + 8 * c) = o; }
;     asm volatile("s_waitcnt lgkmcnt(0)" ::: "memory");
; }
; __device__ __forceinline__ void convert_moe_items(const Ctx& a, int layer, LAS unsigned char* lds, int it0, int it1, int widx, int nw, int wave, int lane) {
;     ...
;     for (;;) {
;         cvt_store(da, va, scr, lane);
;         it += 2 * nw; const bool ha = (it < it1);
;         if (ha) { da = decode(it); cvt_load(da, va, lane); }
.LBB0_1138:
	s_cmp_lg_u64 s[14:15], 0
	s_cbranch_scc1 .Lcvt_p6_t
	s_waitcnt vmcnt(0)
.Lcvt_p6_t:
	v_add_u32_e32 v79, 0x420, v74
	v_add_u32_e32 v80, 0x428, v74
	v_add_u32_e32 v81, 0x840, v74
	v_add_u32_e32 v82, 0x848, v74
	v_add_u32_e32 v83, 0xc60, v74
	v_add_u32_e32 v84, 0xc68, v74
	v_add_u32_e32 v85, 0x1080, v74
	v_add_u32_e32 v86, 0x1088, v74
	v_add_u32_e32 v87, 0x14a0, v74
	v_add_u32_e32 v88, 0x14a8, v74
	v_add_u32_e32 v89, 0x18c0, v74
	v_add_u32_e32 v90, 0x18c8, v74
	v_add_u32_e32 v91, 0x1ce0, v74
	v_add_u32_e32 v92, 0x1ce8, v74
	s_waitcnt vmcnt(15)
	ds_write2_b32 v74, v2, v3 offset1:1
	ds_write2_b32 v74, v4, v5 offset0:2 offset1:3
	s_waitcnt vmcnt(14)
	ds_write2_b32 v79, v6, v7 offset1:1
	ds_write2_b32 v80, v8, v9 offset1:1
	s_waitcnt vmcnt(13)
	ds_write2_b32 v81, v10, v11 offset1:1
	ds_write2_b32 v82, v12, v13 offset1:1
	s_waitcnt vmcnt(12)
	ds_write2_b32 v83, v14, v15 offset1:1
	ds_write2_b32 v84, v16, v17 offset1:1
	s_waitcnt vmcnt(11)
	ds_write2_b32 v85, v18, v19 offset1:1
	ds_write2_b32 v86, v20, v21 offset1:1
	s_waitcnt vmcnt(10)
	ds_write2_b32 v87, v22, v23 offset1:1
	ds_write2_b32 v88, v24, v25 offset1:1
	s_waitcnt vmcnt(9)
	ds_write2_b32 v89, v26, v27 offset1:1
	ds_write2_b32 v90, v28, v29 offset1:1
	s_waitcnt vmcnt(8)
	ds_write2_b32 v91, v30, v31 offset1:1
	ds_write2_b32 v92, v32, v33 offset1:1
	s_waitcnt lgkmcnt(0)
	ds_read2_b32 v[98:99], v73 offset1:8
	ds_read2_b32 v[100:101], v73 offset0:33 offset1:41
	ds_read2_b32 v[102:103], v73 offset0:66 offset1:74
	ds_read2_b32 v[104:105], v73 offset0:99 offset1:107
	ds_read2_b32 v[106:107], v73 offset0:132 offset1:140
	s_waitcnt lgkmcnt(4)
	v_bfe_u32 v67, v98, 16, 1
	v_add3_u32 v67, v98, v67, s41
	s_waitcnt lgkmcnt(3)
	v_bfe_u32 v93, v100, 16, 1
	v_lshrrev_b32_e32 v67, 16, v67
	v_add3_u32 v93, v100, v93, s41
	ds_read2_b32 v[108:109], v73 offset0:165 offset1:173
	v_and_or_b32 v94, v93, s42, v67
	s_waitcnt lgkmcnt(3)
	v_bfe_u32 v67, v102, 16, 1
	v_add3_u32 v67, v102, v67, s41
	s_waitcnt lgkmcnt(2)
	v_bfe_u32 v93, v104, 16, 1
	ds_read2_b32 v[110:111], v73 offset0:198 offset1:206
	v_lshrrev_b32_e32 v67, 16, v67
	v_add3_u32 v93, v104, v93, s41
	ds_read2_b32 v[112:113], v73 offset0:231 offset1:239
	v_and_or_b32 v95, v93, s42, v67
	s_waitcnt lgkmcnt(3)
	v_bfe_u32 v67, v106, 16, 1
	v_add3_u32 v67, v106, v67, s41
	s_waitcnt lgkmcnt(2)
	v_bfe_u32 v93, v108, 16, 1
	v_lshrrev_b32_e32 v67, 16, v67
	v_add3_u32 v93, v108, v93, s41
	v_and_or_b32 v96, v93, s42, v67
	s_waitcnt lgkmcnt(1)
	v_bfe_u32 v67, v110, 16, 1
	v_add3_u32 v67, v110, v67, s41
	s_waitcnt lgkmcnt(0)
	v_bfe_u32 v93, v112, 16, 1
	s_cmp_eq_u32 s25, 0
	v_lshrrev_b32_e32 v67, 16, v67
	v_add3_u32 v93, v112, v93, s41
	s_cselect_b64 vcc, -1, 0
	s_lshl_b32 s2, s12, 1
	v_and_or_b32 v97, v93, s42, v67
	s_and_b32 s13, s2, 0xffffff00
	v_bitop3_b32 v93, s12, v75, v1 bitop3:0xc8
	v_or_b32_e32 v67, s12, v1
	v_or_b32_e32 v93, s13, v93
	v_cndmask_b32_e32 v67, v93, v67, vcc
	v_add_u32_e32 v67, s34, v67
	v_mad_u64_u32 v[114:115], s[2:3], v67, s33, 0
	v_ashrrev_i32_e32 v93, 31, v67
	v_mov_b32_e32 v98, v115
	v_mad_u64_u32 v[116:117], s[2:3], v93, s33, v[98:99]
	v_mov_b32_e32 v115, v116
	s_ashr_i32 s11, s10, 31
	v_lshl_add_u64 v[114:115], v[114:115], 1, s[8:9]
	s_lshl_b64 s[2:3], s[10:11], 1
	v_bfe_u32 v67, v99, 16, 1
	v_lshl_add_u64 v[114:115], v[114:115], 0, s[2:3]
	v_add3_u32 v67, v99, v67, s41
	v_bfe_u32 v93, v101, 16, 1
	v_lshl_add_u64 v[114:115], v[114:115], 0, v[68:69]
	v_lshrrev_b32_e32 v67, 16, v67
	v_add3_u32 v93, v101, v93, s41
	global_store_dwordx4 v[114:115], v[94:97], off nt
	s_add_i32 s44, s35, s39
	s_cmpk_gt_i32 s44, 0x4fff
	v_and_or_b32 v94, v93, s42, v67
	v_bfe_u32 v67, v103, 16, 1
	v_add3_u32 v67, v103, v67, s41
	v_bfe_u32 v93, v105, 16, 1
	v_lshrrev_b32_e32 v67, 16, v67
	v_add3_u32 v93, v105, v93, s41
	v_and_or_b32 v95, v93, s42, v67
	v_bfe_u32 v67, v107, 16, 1
	v_add3_u32 v67, v107, v67, s41
	v_bfe_u32 v93, v109, 16, 1
	v_lshrrev_b32_e32 v67, 16, v67
	v_add3_u32 v93, v109, v93, s41
	v_and_or_b32 v96, v93, s42, v67
	v_bfe_u32 v67, v111, 16, 1
	v_add3_u32 v67, v111, v67, s41
	v_bfe_u32 v93, v113, 16, 1
	v_lshrrev_b32_e32 v67, 16, v67
	v_add3_u32 v93, v113, v93, s41
	v_and_or_b32 v97, v93, s42, v67
	v_bitop3_b32 v93, s12, v76, v70 bitop3:0xc8
	v_or_b32_e32 v67, s12, v70
	v_or_b32_e32 v93, s13, v93
	v_cndmask_b32_e32 v67, v93, v67, vcc
	v_add_u32_e32 v67, s34, v67
	v_mad_u64_u32 v[98:99], s[22:23], v67, s33, 0
	v_ashrrev_i32_e32 v93, 31, v67
	v_mov_b32_e32 v100, v99
	v_mad_u64_u32 v[100:101], s[22:23], v93, s33, v[100:101]
	v_mov_b32_e32 v99, v100
	v_lshl_add_u64 v[98:99], v[98:99], 1, s[8:9]
	v_lshl_add_u64 v[98:99], v[98:99], 0, s[2:3]
	ds_read2_b32 v[100:101], v73 offset0:16 offset1:24
	v_lshl_add_u64 v[98:99], v[98:99], 0, v[68:69]
	global_store_dwordx4 v[98:99], v[94:97], off nt
	ds_read2_b32 v[98:99], v73 offset0:49 offset1:57
	ds_read2_b32 v[102:103], v73 offset0:82 offset1:90
	ds_read2_b32 v[104:105], v73 offset0:115 offset1:123
	s_waitcnt lgkmcnt(3)
; #define LAS __attribute__((address_space(3)))
; __device__ __forceinline__ unsigned pk2(float lo, float hi) { return f2bf(lo) | (f2bf(hi) << 16); }
;     __device__ __forceinline__ const float* x() const { return (const float*)ld(0); }
;     __device__ __forceinline__ const float* c() const { return (const float*)ld(1); }
; template <bool NT = true> __device__ __forceinline__ void cvt_store(const CvtItem& d, const f32x4 (&v)[8], LAS float* scr, int lane) {
;     ...
;     for (int j = 0; j < 4; ++j) { const int n = (lane >> 3) + 8 * j; const LAS float* s = scr + (8 * c) * 33 + n;
;         u32x4 o; o.x = pk2(s[0 * 33], s[1 * 33]); o.y = pk2(s[2 * 33], s[3 * 33]); o.z = pk2(s[4 * 33], s[5 * 33]); o.w = pk2(s[6 * 33], s[7 * 33]);
;         const int ng = d.n0 + n, drow = d.row_off + (d.ilv ? ((ng >> 7) * 256 + (ng & 127)) : ng);
;         if (NT) __builtin_nontemporal_store(o, (u32x4*)(d.dst + (size_t)drow * d.K + d.k0 + 8 * c)); else *(u32x4*)(d.dst + (size_t)drow * d.K + d.k0 + 8 * c) = o; }
;     asm volatile("s_waitcnt lgkmcnt(0)" ::: "memory");
; __device__ __forceinline__ void convert_moe_items(const Ctx& a, int layer, LAS unsigned char* lds, int it0, int it1, int widx, int nw, int wave, int lane) {
;     ...
;     auto decode = [&](int it) { CvtItem d; const int e = it / PER_E; int r = it % PER_E; const size_t eo = ((size_t)layer * NE + e) * (size_t)DM * FE;
;         if (r < I_G)          { d.src = wg + eo; d.dst = WGU; d.N = FE; d.K = DM; d.row_off = e * 2048; d.ilv = 1; }
;         else if (r < 2 * I_G) { r -= I_G; d.src = wu + eo; d.dst = WGU; d.N = FE; d.K = DM; d.row_off = e * 2048 + 128; d.ilv = 1; }
;         else                  { r -= 2 * I_G; d.src = wd + eo; d.dst = WD; d.N = DM; d.K = FE; d.row_off = e * 2048; d.ilv = 0; }
;         const int nblk = d.N / 32; d.k0 = 64 * (r / nblk); d.n0 = 32 * (r % nblk); return d; };
	v_bfe_u32 v67, v100, 16, 1
	v_add3_u32 v67, v100, v67, s41
	s_waitcnt lgkmcnt(2)
	v_bfe_u32 v93, v98, 16, 1
	ds_read2_b32 v[106:107], v73 offset0:148 offset1:156
	v_lshrrev_b32_e32 v67, 16, v67
	v_add3_u32 v93, v98, v93, s41
	ds_read2_b32 v[108:109], v73 offset0:181 offset1:189
	v_and_or_b32 v94, v93, s42, v67
	s_waitcnt lgkmcnt(3)
	v_bfe_u32 v67, v102, 16, 1
	v_add3_u32 v67, v102, v67, s41
	s_waitcnt lgkmcnt(2)
	v_bfe_u32 v93, v104, 16, 1
	ds_read2_b32 v[110:111], v73 offset0:214 offset1:222
	v_lshrrev_b32_e32 v67, 16, v67
	v_add3_u32 v93, v104, v93, s41
	ds_read2_b32 v[112:113], v73 offset0:247 offset1:255
	v_and_or_b32 v95, v93, s42, v67
	s_waitcnt lgkmcnt(3)
	v_bfe_u32 v67, v106, 16, 1
	v_add3_u32 v67, v106, v67, s41
	s_waitcnt lgkmcnt(2)
	v_bfe_u32 v93, v108, 16, 1
	v_lshrrev_b32_e32 v67, 16, v67
	v_add3_u32 v93, v108, v93, s41
	v_and_or_b32 v96, v93, s42, v67
	s_waitcnt lgkmcnt(1)
	v_bfe_u32 v67, v110, 16, 1
	v_add3_u32 v67, v110, v67, s41
	s_waitcnt lgkmcnt(0)
	v_bfe_u32 v93, v112, 16, 1
	v_lshrrev_b32_e32 v67, 16, v67
	v_add3_u32 v93, v112, v93, s41
	v_and_or_b32 v97, v93, s42, v67
	v_bitop3_b32 v93, s12, v77, v71 bitop3:0xc8
	v_or_b32_e32 v67, s12, v71
	v_or_b32_e32 v93, s13, v93
	v_cndmask_b32_e32 v67, v93, v67, vcc
	v_add_u32_e32 v67, s34, v67
	v_mad_u64_u32 v[114:115], s[22:23], v67, s33, 0
	v_ashrrev_i32_e32 v93, 31, v67
	v_mov_b32_e32 v98, v115
	v_mad_u64_u32 v[116:117], s[22:23], v93, s33, v[98:99]
	v_mov_b32_e32 v115, v116
	v_lshl_add_u64 v[114:115], v[114:115], 1, s[8:9]
	v_bfe_u32 v67, v101, 16, 1
	v_lshl_add_u64 v[114:115], v[114:115], 0, s[2:3]
	v_add3_u32 v67, v101, v67, s41
	v_bfe_u32 v93, v99, 16, 1
	v_lshl_add_u64 v[114:115], v[114:115], 0, v[68:69]
	v_lshrrev_b32_e32 v67, 16, v67
	v_add3_u32 v93, v99, v93, s41
	global_store_dwordx4 v[114:115], v[94:97], off nt
	s_nop 1
	v_and_or_b32 v94, v93, s42, v67
	v_bfe_u32 v67, v103, 16, 1
	v_add3_u32 v67, v103, v67, s41
	v_bfe_u32 v93, v105, 16, 1
	v_lshrrev_b32_e32 v67, 16, v67
	v_add3_u32 v93, v105, v93, s41
	v_and_or_b32 v95, v93, s42, v67
	v_bfe_u32 v67, v107, 16, 1
	v_add3_u32 v67, v107, v67, s41
	v_bfe_u32 v93, v109, 16, 1
	v_lshrrev_b32_e32 v67, 16, v67
	v_add3_u32 v93, v109, v93, s41
	v_and_or_b32 v96, v93, s42, v67
	v_bfe_u32 v67, v111, 16, 1
	v_add3_u32 v67, v111, v67, s41
	v_bfe_u32 v93, v113, 16, 1
	v_lshrrev_b32_e32 v67, 16, v67
	v_add3_u32 v93, v113, v93, s41
	v_and_or_b32 v97, v93, s42, v67
	v_bitop3_b32 v93, s12, v78, v72 bitop3:0xc8
	v_or_b32_e32 v67, s12, v72
	v_or_b32_e32 v93, s13, v93
	v_cndmask_b32_e32 v67, v93, v67, vcc
	v_add_u32_e32 v67, s34, v67
	v_mad_u64_u32 v[98:99], s[22:23], v67, s33, 0
	v_ashrrev_i32_e32 v93, 31, v67
	v_mov_b32_e32 v100, v99
	v_mad_u64_u32 v[100:101], s[22:23], v93, s33, v[100:101]
	v_mov_b32_e32 v99, v100
	v_lshl_add_u64 v[98:99], v[98:99], 1, s[8:9]
	v_lshl_add_u64 v[98:99], v[98:99], 0, s[2:3]
	v_lshl_add_u64 v[98:99], v[98:99], 0, v[68:69]
	global_store_dwordx4 v[98:99], v[94:97], off nt
	s_waitcnt lgkmcnt(0)
	s_cselect_b64 s[22:23], -1, 0
	s_and_b64 vcc, exec, s[22:23]
	s_cbranch_vccnz .LBB0_1147
	s_mul_hi_i32 s2, s44, 0x2aaaaaab
	s_lshr_b32 s3, s2, 31
	s_ashr_i32 s2, s2, 9
	s_add_i32 s24, s2, s3
	s_mul_i32 s2, s24, 0xfffff400
	s_ashr_i32 s25, s24, 31
	s_add_i32 s21, s44, s2
	s_lshl_b64 s[10:11], s[24:25], 21
	s_lshl_b32 s45, s24, 11
	s_cmpk_gt_i32 s21, 0x3ff
	s_mov_b64 s[12:13], -1
	s_cbranch_scc0 .LBB0_1144
	s_mul_i32 s2, s24, 0xc00
	s_sub_i32 s12, s44, s2
	s_cmpk_gt_u32 s21, 0x7ff
	s_mov_b64 s[8:9], -1
	s_cbranch_scc0 .LBB0_1142
	s_add_i32 s19, s12, 0xfffff800
	s_lshl_b64 s[2:3], s[10:11], 2
	s_add_u32 s2, s31, s2
	s_addc_u32 s3, s30, s3
	s_mov_b64 s[8:9], 0

; #define LAS __attribute__((address_space(3)))
; __device__ __forceinline__ unsigned pk2(float lo, float hi) { return f2bf(lo) | (f2bf(hi) << 16); }
;     __device__ __forceinline__ const float* x() const { return (const float*)ld(0); }
;     __device__ __forceinline__ const float* c() const { return (const float*)ld(1); }
; template <bool NT = true> __device__ __forceinline__ void cvt_store(const CvtItem& d, const f32x4 (&v)[8], LAS float* scr, int lane) {
;     const int rr = lane >> 3, c4 = (lane & 7) * 4;
; #pragma unroll
;     for (int q = 0; q < 8; ++q) { LAS float* t = scr + (8 * q + rr) * 33 + c4; t[0] = v[q].x; t[1] = v[q].y; t[2] = v[q].z; t[3] = v[q].w; }
;     asm volatile("s_waitcnt lgkmcnt(0)" ::: "memory");
;     const int c = lane & 7;
; #pragma unroll
;     for (int j = 0; j < 4; ++j) { const int n = (lane >> 3) + 8 * j; const LAS float* s = scr + (8 * c) * 33 + n;
;         u32x4 o; o.x = pk2(s[0 * 33], s[1 * 33]); o.y = pk2(s[2 * 33], s[3 * 33]); o.z = pk2(s[4 * 33], s[5 * 33]); o.w = pk2(s[6 * 33], s[7 * 33]);
;         const int ng = d.n0 + n, drow = d.row_off + (d.ilv ? ((ng >> 7) * 256 + (ng & 127)) : ng);
;         if (NT) __builtin_nontemporal_store(o, (u32x4*)(d.dst + (size_t)drow * d.K + d.k0 + 8 * c)); else *(u32x4*)(d.dst + (size_t)drow * d.K + d.k0 + 8 * c) = o; }
;     asm volatile("s_waitcnt lgkmcnt(0)" ::: "memory");
; }
; __device__ __forceinline__ void convert_moe_items(const Ctx& a, int layer, LAS unsigned char* lds, int it0, int it1, int widx, int nw, int wave, int lane) {
;     ...
;         cvt_store(db, vb, scr, lane);
;         hb = (it + nw < it1);
;         if (hb) { db = decode(it + nw); cvt_load(db, vb, lane); }
.LBB0_1148:
	s_cmp_lg_u64 s[22:23], 0
	s_cbranch_scc0 .Lcvt_p6_m
	s_waitcnt vmcnt(0)
.Lcvt_p6_m:
	s_waitcnt vmcnt(12)
	ds_write2_b32 v74, v34, v35 offset1:1
	ds_write2_b32 v74, v36, v37 offset0:2 offset1:3
	ds_write2_b32 v79, v38, v39 offset1:1
	ds_write2_b32 v80, v40, v41 offset1:1
	ds_write2_b32 v81, v42, v43 offset1:1
	ds_write2_b32 v82, v44, v45 offset1:1
	ds_write2_b32 v83, v46, v47 offset1:1
	ds_write2_b32 v84, v48, v49 offset1:1
	ds_write2_b32 v85, v50, v51 offset1:1
	ds_write2_b32 v86, v52, v53 offset1:1
	ds_write2_b32 v87, v54, v55 offset1:1
	ds_write2_b32 v88, v56, v57 offset1:1
	ds_write2_b32 v89, v58, v59 offset1:1
	ds_write2_b32 v90, v60, v61 offset1:1
	ds_write2_b32 v91, v62, v63 offset1:1
	ds_write2_b32 v92, v64, v65 offset1:1
	s_waitcnt lgkmcnt(0)
	ds_read2_b32 v[84:85], v73 offset1:8
	ds_read2_b32 v[86:87], v73 offset0:33 offset1:41
	ds_read2_b32 v[88:89], v73 offset0:66 offset1:74
	ds_read2_b32 v[90:91], v73 offset0:99 offset1:107
	ds_read2_b32 v[92:93], v73 offset0:132 offset1:140
	s_waitcnt lgkmcnt(4)
	v_bfe_u32 v67, v84, 16, 1
	v_add3_u32 v67, v84, v67, s41
	s_waitcnt lgkmcnt(3)
	v_bfe_u32 v79, v86, 16, 1
	v_lshrrev_b32_e32 v67, 16, v67
	v_add3_u32 v79, v86, v79, s41
	ds_read2_b32 v[94:95], v73 offset0:165 offset1:173
	v_and_or_b32 v80, v79, s42, v67
	s_waitcnt lgkmcnt(3)
	v_bfe_u32 v67, v88, 16, 1
	v_add3_u32 v67, v88, v67, s41
	s_waitcnt lgkmcnt(2)
	v_bfe_u32 v79, v90, 16, 1
	ds_read2_b32 v[96:97], v73 offset0:198 offset1:206
	v_lshrrev_b32_e32 v67, 16, v67
	v_add3_u32 v79, v90, v79, s41
	ds_read2_b32 v[98:99], v73 offset0:231 offset1:239
	v_and_or_b32 v81, v79, s42, v67
	s_waitcnt lgkmcnt(3)
	v_bfe_u32 v67, v92, 16, 1
	v_add3_u32 v67, v92, v67, s41
	s_waitcnt lgkmcnt(2)
	v_bfe_u32 v79, v94, 16, 1
	v_lshrrev_b32_e32 v67, 16, v67
	v_add3_u32 v79, v94, v79, s41
	v_and_or_b32 v82, v79, s42, v67
	s_waitcnt lgkmcnt(1)
	v_bfe_u32 v67, v96, 16, 1
	v_add3_u32 v67, v96, v67, s41
	s_waitcnt lgkmcnt(0)
	v_bfe_u32 v79, v98, 16, 1
	v_lshrrev_b32_e32 v67, 16, v67
	v_add3_u32 v79, v98, v79, s41
	v_and_or_b32 v83, v79, s42, v67
	v_add_u32_e32 v67, s20, v1
	s_cmp_eq_u32 s36, 0
	v_lshlrev_b32_e32 v79, 1, v67
	v_and_b32_e32 v84, 0x7f, v67
	v_and_or_b32 v79, v79, s43, v84
	s_cselect_b64 vcc, -1, 0
	v_cndmask_b32_e32 v67, v79, v67, vcc
	v_add_u32_e32 v67, s38, v67
	v_mad_u64_u32 v[100:101], s[2:3], v67, s37, 0
	v_ashrrev_i32_e32 v79, 31, v67
	v_mov_b32_e32 v84, v101
	v_mad_u64_u32 v[102:103], s[2:3], v79, s37, v[84:85]
	v_mov_b32_e32 v101, v102
	s_ashr_i32 s19, s18, 31
	v_lshl_add_u64 v[100:101], v[100:101], 1, s[0:1]
	s_lshl_b64 s[2:3], s[18:19], 1
	v_bfe_u32 v67, v85, 16, 1
	v_lshl_add_u64 v[100:101], v[100:101], 0, s[2:3]
	v_add3_u32 v67, v85, v67, s41
	v_bfe_u32 v79, v87, 16, 1
	v_lshl_add_u64 v[100:101], v[100:101], 0, v[68:69]
	v_lshrrev_b32_e32 v67, 16, v67
	v_add3_u32 v79, v87, v79, s41
	global_store_dwordx4 v[100:101], v[80:83], off nt
	s_nop 1
	v_and_or_b32 v80, v79, s42, v67
	v_bfe_u32 v67, v89, 16, 1
	v_add3_u32 v67, v89, v67, s41
	v_bfe_u32 v79, v91, 16, 1
	v_lshrrev_b32_e32 v67, 16, v67
	v_add3_u32 v79, v91, v79, s41
	v_and_or_b32 v81, v79, s42, v67
	v_bfe_u32 v67, v93, 16, 1
	v_add3_u32 v67, v93, v67, s41
	v_bfe_u32 v79, v95, 16, 1
	v_lshrrev_b32_e32 v67, 16, v67
	v_add3_u32 v79, v95, v79, s41
	v_and_or_b32 v82, v79, s42, v67
	v_bfe_u32 v67, v97, 16, 1
	v_add3_u32 v67, v97, v67, s41
	v_bfe_u32 v79, v99, 16, 1
	v_lshrrev_b32_e32 v67, 16, v67
	v_add3_u32 v79, v99, v79, s41
	v_and_or_b32 v83, v79, s42, v67
	v_add_u32_e32 v67, s20, v70
	v_lshlrev_b32_e32 v79, 1, v67
	v_and_b32_e32 v84, 0x7f, v67
	v_and_or_b32 v79, v79, s43, v84
	v_cndmask_b32_e32 v67, v79, v67, vcc
	v_add_u32_e32 v67, s38, v67
	v_mad_u64_u32 v[84:85], s[14:15], v67, s37, 0
	v_ashrrev_i32_e32 v79, 31, v67
	v_mov_b32_e32 v86, v85
	v_mad_u64_u32 v[86:87], s[14:15], v79, s37, v[86:87]
	v_mov_b32_e32 v85, v86
	v_lshl_add_u64 v[84:85], v[84:85], 1, s[0:1]
	v_lshl_add_u64 v[84:85], v[84:85], 0, s[2:3]
	ds_read2_b32 v[86:87], v73 offset0:16 offset1:24
	v_lshl_add_u64 v[84:85], v[84:85], 0, v[68:69]
	global_store_dwordx4 v[84:85], v[80:83], off nt
	ds_read2_b32 v[84:85], v73 offset0:49 offset1:57
	ds_read2_b32 v[88:89], v73 offset0:82 offset1:90
	ds_read2_b32 v[90:91], v73 offset0:115 offset1:123
	s_waitcnt lgkmcnt(3)
; #define LAS __attribute__((address_space(3)))
; __device__ __forceinline__ unsigned pk2(float lo, float hi) { return f2bf(lo) | (f2bf(hi) << 16); }
;     __device__ __forceinline__ const float* x() const { return (const float*)ld(0); }
;     __device__ __forceinline__ const float* c() const { return (const float*)ld(1); }
; template <bool NT = true> __device__ __forceinline__ void cvt_store(const CvtItem& d, const f32x4 (&v)[8], LAS float* scr, int lane) {
;     ...
;     for (int j = 0; j < 4; ++j) { const int n = (lane >> 3) + 8 * j; const LAS float* s = scr + (8 * c) * 33 + n;
;         u32x4 o; o.x = pk2(s[0 * 33], s[1 * 33]); o.y = pk2(s[2 * 33], s[3 * 33]); o.z = pk2(s[4 * 33], s[5 * 33]); o.w = pk2(s[6 * 33], s[7 * 33]);
;         const int ng = d.n0 + n, drow = d.row_off + (d.ilv ? ((ng >> 7) * 256 + (ng & 127)) : ng);
;         if (NT) __builtin_nontemporal_store(o, (u32x4*)(d.dst + (size_t)drow * d.K + d.k0 + 8 * c)); else *(u32x4*)(d.dst + (size_t)drow * d.K + d.k0 + 8 * c) = o; }
;     asm volatile("s_waitcnt lgkmcnt(0)" ::: "memory");
; __device__ __forceinline__ void convert_moe_items(const Ctx& a, int layer, LAS unsigned char* lds, int it0, int it1, int widx, int nw, int wave, int lane) {
;     ...
;     auto decode = [&](int it) { CvtItem d; const int e = it / PER_E; int r = it % PER_E; const size_t eo = ((size_t)layer * NE + e) * (size_t)DM * FE;
;         if (r < I_G)          { d.src = wg + eo; d.dst = WGU; d.N = FE; d.K = DM; d.row_off = e * 2048; d.ilv = 1; }
;         else if (r < 2 * I_G) { r -= I_G; d.src = wu + eo; d.dst = WGU; d.N = FE; d.K = DM; d.row_off = e * 2048 + 128; d.ilv = 1; }
;         else                  { r -= 2 * I_G; d.src = wd + eo; d.dst = WD; d.N = DM; d.K = FE; d.row_off = e * 2048; d.ilv = 0; }
;         const int nblk = d.N / 32; d.k0 = 64 * (r / nblk); d.n0 = 32 * (r % nblk); return d; };
;     ...
;         hb = (it + nw < it1);
;         if (hb) { db = decode(it + nw); cvt_load(db, vb, lane); }
;         if (!ha) break;
;     }
	v_bfe_u32 v67, v86, 16, 1
	v_add3_u32 v67, v86, v67, s41
	s_waitcnt lgkmcnt(2)
	v_bfe_u32 v79, v84, 16, 1
	ds_read2_b32 v[92:93], v73 offset0:148 offset1:156
	v_lshrrev_b32_e32 v67, 16, v67
	v_add3_u32 v79, v84, v79, s41
	ds_read2_b32 v[94:95], v73 offset0:181 offset1:189
	v_and_or_b32 v80, v79, s42, v67
	s_waitcnt lgkmcnt(3)
	v_bfe_u32 v67, v88, 16, 1
	v_add3_u32 v67, v88, v67, s41
	s_waitcnt lgkmcnt(2)
	v_bfe_u32 v79, v90, 16, 1
	ds_read2_b32 v[96:97], v73 offset0:214 offset1:222
	v_lshrrev_b32_e32 v67, 16, v67
	v_add3_u32 v79, v90, v79, s41
	ds_read2_b32 v[98:99], v73 offset0:247 offset1:255
	v_and_or_b32 v81, v79, s42, v67
	s_waitcnt lgkmcnt(3)
	v_bfe_u32 v67, v92, 16, 1
	v_add3_u32 v67, v92, v67, s41
	s_waitcnt lgkmcnt(2)
	v_bfe_u32 v79, v94, 16, 1
	v_lshrrev_b32_e32 v67, 16, v67
	v_add3_u32 v79, v94, v79, s41
	v_and_or_b32 v82, v79, s42, v67
	s_waitcnt lgkmcnt(1)
	v_bfe_u32 v67, v96, 16, 1
	v_add3_u32 v67, v96, v67, s41
	s_waitcnt lgkmcnt(0)
	v_bfe_u32 v79, v98, 16, 1
	v_lshrrev_b32_e32 v67, 16, v67
	v_add3_u32 v79, v98, v79, s41
	v_and_or_b32 v83, v79, s42, v67
	v_add_u32_e32 v67, s20, v71
	v_lshlrev_b32_e32 v79, 1, v67
	v_and_b32_e32 v84, 0x7f, v67
	v_and_or_b32 v79, v79, s43, v84
	v_cndmask_b32_e32 v67, v79, v67, vcc
	v_add_u32_e32 v67, s38, v67
	v_mad_u64_u32 v[100:101], s[14:15], v67, s37, 0
	v_ashrrev_i32_e32 v79, 31, v67
	v_mov_b32_e32 v84, v101
	v_mad_u64_u32 v[102:103], s[14:15], v79, s37, v[84:85]
	v_mov_b32_e32 v101, v102
	v_lshl_add_u64 v[100:101], v[100:101], 1, s[0:1]
	v_bfe_u32 v67, v87, 16, 1
	v_lshl_add_u64 v[100:101], v[100:101], 0, s[2:3]
	v_add3_u32 v67, v87, v67, s41
	v_bfe_u32 v79, v85, 16, 1
	v_lshl_add_u64 v[100:101], v[100:101], 0, v[68:69]
	v_lshrrev_b32_e32 v67, 16, v67
	v_add3_u32 v79, v85, v79, s41
	global_store_dwordx4 v[100:101], v[80:83], off nt
	s_nop 1
	v_and_or_b32 v80, v79, s42, v67
	v_bfe_u32 v67, v89, 16, 1
	v_add3_u32 v67, v89, v67, s41
	v_bfe_u32 v79, v91, 16, 1
	v_lshrrev_b32_e32 v67, 16, v67
	v_add3_u32 v79, v91, v79, s41
	v_and_or_b32 v81, v79, s42, v67
	v_bfe_u32 v67, v93, 16, 1
	v_add3_u32 v67, v93, v67, s41
	v_bfe_u32 v79, v95, 16, 1
	v_lshrrev_b32_e32 v67, 16, v67
	v_add3_u32 v79, v95, v79, s41
	v_and_or_b32 v82, v79, s42, v67
	v_bfe_u32 v67, v97, 16, 1
	v_add3_u32 v67, v97, v67, s41
	v_bfe_u32 v79, v99, 16, 1
	v_lshrrev_b32_e32 v67, 16, v67
	v_add3_u32 v79, v99, v79, s41
	v_and_or_b32 v83, v79, s42, v67
	v_add_u32_e32 v67, s20, v72
	v_lshlrev_b32_e32 v79, 1, v67
	v_and_b32_e32 v84, 0x7f, v67
	v_and_or_b32 v79, v79, s43, v84
	v_cndmask_b32_e32 v67, v79, v67, vcc
	v_add_u32_e32 v67, s38, v67
	v_mad_u64_u32 v[84:85], s[14:15], v67, s37, 0
	v_ashrrev_i32_e32 v79, 31, v67
	v_mov_b32_e32 v86, v85
	v_mad_u64_u32 v[86:87], s[14:15], v79, s37, v[86:87]
	v_mov_b32_e32 v85, v86
	v_lshl_add_u64 v[84:85], v[84:85], 1, s[0:1]
	v_lshl_add_u64 v[84:85], v[84:85], 0, s[2:3]
	v_lshl_add_u64 v[84:85], v[84:85], 0, v[68:69]
	global_store_dwordx4 v[84:85], v[80:83], off nt
	s_add_i32 s2, s40, s35
	s_waitcnt lgkmcnt(0)
	s_cmpk_lt_i32 s2, 0x5000
	s_cselect_b64 s[14:15], -1, 0
	s_cmpk_gt_i32 s2, 0x4fff
	s_cbranch_scc1 .LBB0_1136
	s_mul_hi_i32 s0, s2, 0x2aaaaaab
	s_lshr_b32 s1, s0, 31
	s_ashr_i32 s0, s0, 9
	s_add_i32 s0, s0, s1
	s_mul_i32 s1, s0, 0xc00
	s_sub_i32 s13, s2, s1
	s_ashr_i32 s1, s0, 31
	s_lshl_b64 s[18:19], s[0:1], 21
	s_lshl_b32 s24, s0, 11
	s_cmpk_gt_i32 s13, 0x3ff
	s_mov_b64 s[20:21], -1
	s_cbranch_scc0 .LBB0_1154
	s_cmpk_gt_u32 s13, 0x7ff
	s_mov_b64 s[0:1], -1
	s_cbranch_scc0 .LBB0_1152
	s_add_i32 s11, s13, 0xfffff800
	s_lshl_b64 s[0:1], s[18:19], 2
	s_add_u32 s2, s31, s0
	s_addc_u32 s3, s30, s1
	s_mov_b64 s[0:1], 0

; #define LAS __attribute__((address_space(3)))
; __device__ __forceinline__ unsigned pk2(float lo, float hi) { return f2bf(lo) | (f2bf(hi) << 16); }
;     __device__ __forceinline__ const float* x() const { return (const float*)ld(0); }
;     __device__ __forceinline__ const float* c() const { return (const float*)ld(1); }
; template <bool NT = true> __device__ __forceinline__ void cvt_store(const CvtItem& d, const f32x4 (&v)[8], LAS float* scr, int lane) {
;     const int rr = lane >> 3, c4 = (lane & 7) * 4;
; #pragma unroll
;     for (int q = 0; q < 8; ++q) { LAS float* t = scr + (8 * q + rr) * 33 + c4; t[0] = v[q].x; t[1] = v[q].y; t[2] = v[q].z; t[3] = v[q].w; }
;     asm volatile("s_waitcnt lgkmcnt(0)" ::: "memory");
;     const int c = lane & 7;
; #pragma unroll
;     for (int j = 0; j < 4; ++j) { const int n = (lane >> 3) + 8 * j; const LAS float* s = scr + (8 * c) * 33 + n;
;         u32x4 o; o.x = pk2(s[0 * 33], s[1 * 33]); o.y = pk2(s[2 * 33], s[3 * 33]); o.z = pk2(s[4 * 33], s[5 * 33]); o.w = pk2(s[6 * 33], s[7 * 33]);
;         const int ng = d.n0 + n, drow = d.row_off + (d.ilv ? ((ng >> 7) * 256 + (ng & 127)) : ng);
;         if (NT) __builtin_nontemporal_store(o, (u32x4*)(d.dst + (size_t)drow * d.K + d.k0 + 8 * c)); else *(u32x4*)(d.dst + (size_t)drow * d.K + d.k0 + 8 * c) = o; }
;     asm volatile("s_waitcnt lgkmcnt(0)" ::: "memory");
; }
; __device__ __forceinline__ void convert_moe_items(const Ctx& a, int layer, LAS unsigned char* lds, int it0, int it1, int widx, int nw, int wave, int lane) {
;     ...
;     for (;;) {
;         cvt_store(da, va, scr, lane);
;         it += 2 * nw; const bool ha = (it < it1);
;         if (ha) { da = decode(it); cvt_load(da, va, lane); }
.Lcvt_p15_t:
	v_add_u32_e32 v79, 0x420, v74
	v_add_u32_e32 v80, 0x428, v74
	v_add_u32_e32 v81, 0x840, v74
	v_add_u32_e32 v82, 0x848, v74
	v_add_u32_e32 v83, 0xc60, v74
	v_add_u32_e32 v84, 0xc68, v74
	v_add_u32_e32 v85, 0x1080, v74
	v_add_u32_e32 v86, 0x1088, v74
	v_add_u32_e32 v87, 0x14a0, v74
	v_add_u32_e32 v88, 0x14a8, v74
	v_add_u32_e32 v89, 0x18c0, v74
	v_add_u32_e32 v90, 0x18c8, v74
	v_add_u32_e32 v91, 0x1ce0, v74
	v_add_u32_e32 v92, 0x1ce8, v74
	s_waitcnt vmcnt(15)
	ds_write2_b32 v74, v2, v3 offset1:1
	ds_write2_b32 v74, v4, v5 offset0:2 offset1:3
	s_waitcnt vmcnt(14)
	ds_write2_b32 v79, v6, v7 offset1:1
	ds_write2_b32 v80, v8, v9 offset1:1
	s_waitcnt vmcnt(13)
	ds_write2_b32 v81, v10, v11 offset1:1
	ds_write2_b32 v82, v12, v13 offset1:1
	s_waitcnt vmcnt(12)
	ds_write2_b32 v83, v14, v15 offset1:1
	ds_write2_b32 v84, v16, v17 offset1:1
	s_waitcnt vmcnt(11)
	ds_write2_b32 v85, v18, v19 offset1:1
	ds_write2_b32 v86, v20, v21 offset1:1
	s_waitcnt vmcnt(10)
	ds_write2_b32 v87, v22, v23 offset1:1
	ds_write2_b32 v88, v24, v25 offset1:1
	s_waitcnt vmcnt(9)
	ds_write2_b32 v89, v26, v27 offset1:1
	ds_write2_b32 v90, v28, v29 offset1:1
	s_waitcnt vmcnt(8)
	ds_write2_b32 v91, v30, v31 offset1:1
	ds_write2_b32 v92, v32, v33 offset1:1
	s_waitcnt lgkmcnt(0)
	ds_read2_b32 v[98:99], v73 offset1:8
	ds_read2_b32 v[100:101], v73 offset0:33 offset1:41
	ds_read2_b32 v[102:103], v73 offset0:66 offset1:74
	ds_read2_b32 v[104:105], v73 offset0:99 offset1:107
	ds_read2_b32 v[106:107], v73 offset0:132 offset1:140
	s_waitcnt lgkmcnt(4)
	v_bfe_u32 v67, v98, 16, 1
	v_add3_u32 v67, v98, v67, s41
	s_waitcnt lgkmcnt(3)
	v_bfe_u32 v93, v100, 16, 1
	v_lshrrev_b32_e32 v67, 16, v67
	v_add3_u32 v93, v100, v93, s41
	ds_read2_b32 v[108:109], v73 offset0:165 offset1:173
	v_and_or_b32 v94, v93, s42, v67
	s_waitcnt lgkmcnt(3)
	v_bfe_u32 v67, v102, 16, 1
	v_add3_u32 v67, v102, v67, s41
	s_waitcnt lgkmcnt(2)
	v_bfe_u32 v93, v104, 16, 1
	ds_read2_b32 v[110:111], v73 offset0:198 offset1:206
	v_lshrrev_b32_e32 v67, 16, v67
	v_add3_u32 v93, v104, v93, s41
	ds_read2_b32 v[112:113], v73 offset0:231 offset1:239
	v_and_or_b32 v95, v93, s42, v67
	s_waitcnt lgkmcnt(3)
	v_bfe_u32 v67, v106, 16, 1
	v_add3_u32 v67, v106, v67, s41
	s_waitcnt lgkmcnt(2)
	v_bfe_u32 v93, v108, 16, 1
	v_lshrrev_b32_e32 v67, 16, v67
	v_add3_u32 v93, v108, v93, s41
	v_and_or_b32 v96, v93, s42, v67
	s_waitcnt lgkmcnt(1)
	v_bfe_u32 v67, v110, 16, 1
	v_add3_u32 v67, v110, v67, s41
	s_waitcnt lgkmcnt(0)
	v_bfe_u32 v93, v112, 16, 1
	s_cmp_eq_u32 s25, 0
	v_lshrrev_b32_e32 v67, 16, v67
	v_add3_u32 v93, v112, v93, s41
	s_cselect_b64 vcc, -1, 0
	s_lshl_b32 s2, s10, 1
	v_and_or_b32 v97, v93, s42, v67
	s_and_b32 s11, s2, 0xffffff00
	v_bitop3_b32 v93, s10, v75, v1 bitop3:0xc8
	v_or_b32_e32 v67, s10, v1
	v_or_b32_e32 v93, s11, v93
	v_cndmask_b32_e32 v67, v93, v67, vcc
	v_add_u32_e32 v67, s34, v67
	v_mad_u64_u32 v[114:115], s[2:3], v67, s33, 0
	v_ashrrev_i32_e32 v93, 31, v67
	v_mov_b32_e32 v98, v115
	v_mad_u64_u32 v[116:117], s[2:3], v93, s33, v[98:99]
	v_mov_b32_e32 v115, v116
	s_ashr_i32 s9, s8, 31
	v_lshl_add_u64 v[114:115], v[114:115], 1, s[6:7]
	s_lshl_b64 s[2:3], s[8:9], 1
	v_bfe_u32 v67, v99, 16, 1
	v_lshl_add_u64 v[114:115], v[114:115], 0, s[2:3]
	v_add3_u32 v67, v99, v67, s41
	v_bfe_u32 v93, v101, 16, 1
	v_lshl_add_u64 v[114:115], v[114:115], 0, v[68:69]
	v_lshrrev_b32_e32 v67, 16, v67
	v_add3_u32 v93, v101, v93, s41
	global_store_dwordx4 v[114:115], v[94:97], off nt
	s_add_i32 s44, s35, s39
	s_cmp_gt_i32 s44, 0xbfff
	v_and_or_b32 v94, v93, s42, v67
	v_bfe_u32 v67, v103, 16, 1
	v_add3_u32 v67, v103, v67, s41
	v_bfe_u32 v93, v105, 16, 1
	v_lshrrev_b32_e32 v67, 16, v67
	v_add3_u32 v93, v105, v93, s41
	v_and_or_b32 v95, v93, s42, v67
	v_bfe_u32 v67, v107, 16, 1
	v_add3_u32 v67, v107, v67, s41
	v_bfe_u32 v93, v109, 16, 1
	v_lshrrev_b32_e32 v67, 16, v67
	v_add3_u32 v93, v109, v93, s41
	v_and_or_b32 v96, v93, s42, v67
	v_bfe_u32 v67, v111, 16, 1
	v_add3_u32 v67, v111, v67, s41
	v_bfe_u32 v93, v113, 16, 1
	v_lshrrev_b32_e32 v67, 16, v67
	v_add3_u32 v93, v113, v93, s41
	v_and_or_b32 v97, v93, s42, v67
	v_bitop3_b32 v93, s10, v76, v70 bitop3:0xc8
	v_or_b32_e32 v67, s10, v70
	v_or_b32_e32 v93, s11, v93
	v_cndmask_b32_e32 v67, v93, v67, vcc
	v_add_u32_e32 v67, s34, v67
	v_mad_u64_u32 v[98:99], s[22:23], v67, s33, 0
	v_ashrrev_i32_e32 v93, 31, v67
	v_mov_b32_e32 v100, v99
	v_mad_u64_u32 v[100:101], s[22:23], v93, s33, v[100:101]
	v_mov_b32_e32 v99, v100
	v_lshl_add_u64 v[98:99], v[98:99], 1, s[6:7]
	v_lshl_add_u64 v[98:99], v[98:99], 0, s[2:3]
	ds_read2_b32 v[100:101], v73 offset0:16 offset1:24
	v_lshl_add_u64 v[98:99], v[98:99], 0, v[68:69]
	global_store_dwordx4 v[98:99], v[94:97], off nt
	ds_read2_b32 v[98:99], v73 offset0:49 offset1:57
	ds_read2_b32 v[102:103], v73 offset0:82 offset1:90
	ds_read2_b32 v[104:105], v73 offset0:115 offset1:123
	s_waitcnt lgkmcnt(3)
; #define LAS __attribute__((address_space(3)))
; __device__ __forceinline__ unsigned pk2(float lo, float hi) { return f2bf(lo) | (f2bf(hi) << 16); }
;     __device__ __forceinline__ const float* x() const { return (const float*)ld(0); }
;     __device__ __forceinline__ const float* c() const { return (const float*)ld(1); }
; template <bool NT = true> __device__ __forceinline__ void cvt_store(const CvtItem& d, const f32x4 (&v)[8], LAS float* scr, int lane) {
;     ...
;     for (int j = 0; j < 4; ++j) { const int n = (lane >> 3) + 8 * j; const LAS float* s = scr + (8 * c) * 33 + n;
;         u32x4 o; o.x = pk2(s[0 * 33], s[1 * 33]); o.y = pk2(s[2 * 33], s[3 * 33]); o.z = pk2(s[4 * 33], s[5 * 33]); o.w = pk2(s[6 * 33], s[7 * 33]);
;         const int ng = d.n0 + n, drow = d.row_off + (d.ilv ? ((ng >> 7) * 256 + (ng & 127)) : ng);
;         if (NT) __builtin_nontemporal_store(o, (u32x4*)(d.dst + (size_t)drow * d.K + d.k0 + 8 * c)); else *(u32x4*)(d.dst + (size_t)drow * d.K + d.k0 + 8 * c) = o; }
;     asm volatile("s_waitcnt lgkmcnt(0)" ::: "memory");
; __device__ __forceinline__ void convert_moe_items(const Ctx& a, int layer, LAS unsigned char* lds, int it0, int it1, int widx, int nw, int wave, int lane) {
;     ...
;     auto decode = [&](int it) { CvtItem d; const int e = it / PER_E; int r = it % PER_E; const size_t eo = ((size_t)layer * NE + e) * (size_t)DM * FE;
;         if (r < I_G)          { d.src = wg + eo; d.dst = WGU; d.N = FE; d.K = DM; d.row_off = e * 2048; d.ilv = 1; }
;         else if (r < 2 * I_G) { r -= I_G; d.src = wu + eo; d.dst = WGU; d.N = FE; d.K = DM; d.row_off = e * 2048 + 128; d.ilv = 1; }
;         else                  { r -= 2 * I_G; d.src = wd + eo; d.dst = WD; d.N = DM; d.K = FE; d.row_off = e * 2048; d.ilv = 0; }
;         const int nblk = d.N / 32; d.k0 = 64 * (r / nblk); d.n0 = 32 * (r % nblk); return d; };
	v_bfe_u32 v67, v100, 16, 1
	v_add3_u32 v67, v100, v67, s41
	s_waitcnt lgkmcnt(2)
	v_bfe_u32 v93, v98, 16, 1
	ds_read2_b32 v[106:107], v73 offset0:148 offset1:156
	v_lshrrev_b32_e32 v67, 16, v67
	v_add3_u32 v93, v98, v93, s41
	ds_read2_b32 v[108:109], v73 offset0:181 offset1:189
	v_and_or_b32 v94, v93, s42, v67
	s_waitcnt lgkmcnt(3)
	v_bfe_u32 v67, v102, 16, 1
	v_add3_u32 v67, v102, v67, s41
	s_waitcnt lgkmcnt(2)
	v_bfe_u32 v93, v104, 16, 1
	ds_read2_b32 v[110:111], v73 offset0:214 offset1:222
	v_lshrrev_b32_e32 v67, 16, v67
	v_add3_u32 v93, v104, v93, s41
	ds_read2_b32 v[112:113], v73 offset0:247 offset1:255
	v_and_or_b32 v95, v93, s42, v67
	s_waitcnt lgkmcnt(3)
	v_bfe_u32 v67, v106, 16, 1
	v_add3_u32 v67, v106, v67, s41
	s_waitcnt lgkmcnt(2)
	v_bfe_u32 v93, v108, 16, 1
	v_lshrrev_b32_e32 v67, 16, v67
	v_add3_u32 v93, v108, v93, s41
	v_and_or_b32 v96, v93, s42, v67
	s_waitcnt lgkmcnt(1)
	v_bfe_u32 v67, v110, 16, 1
	v_add3_u32 v67, v110, v67, s41
	s_waitcnt lgkmcnt(0)
	v_bfe_u32 v93, v112, 16, 1
	v_lshrrev_b32_e32 v67, 16, v67
	v_add3_u32 v93, v112, v93, s41
	v_and_or_b32 v97, v93, s42, v67
	v_bitop3_b32 v93, s10, v77, v71 bitop3:0xc8
	v_or_b32_e32 v67, s10, v71
	v_or_b32_e32 v93, s11, v93
	v_cndmask_b32_e32 v67, v93, v67, vcc
	v_add_u32_e32 v67, s34, v67
	v_mad_u64_u32 v[114:115], s[22:23], v67, s33, 0
	v_ashrrev_i32_e32 v93, 31, v67
	v_mov_b32_e32 v98, v115
	v_mad_u64_u32 v[116:117], s[22:23], v93, s33, v[98:99]
	v_mov_b32_e32 v115, v116
	v_lshl_add_u64 v[114:115], v[114:115], 1, s[6:7]
	v_bfe_u32 v67, v101, 16, 1
	v_lshl_add_u64 v[114:115], v[114:115], 0, s[2:3]
	v_add3_u32 v67, v101, v67, s41
	v_bfe_u32 v93, v99, 16, 1
	v_lshl_add_u64 v[114:115], v[114:115], 0, v[68:69]
	v_lshrrev_b32_e32 v67, 16, v67
	v_add3_u32 v93, v99, v93, s41
	global_store_dwordx4 v[114:115], v[94:97], off nt
	s_nop 1
	v_and_or_b32 v94, v93, s42, v67
	v_bfe_u32 v67, v103, 16, 1
	v_add3_u32 v67, v103, v67, s41
	v_bfe_u32 v93, v105, 16, 1
	v_lshrrev_b32_e32 v67, 16, v67
	v_add3_u32 v93, v105, v93, s41
	v_and_or_b32 v95, v93, s42, v67
	v_bfe_u32 v67, v107, 16, 1
	v_add3_u32 v67, v107, v67, s41
	v_bfe_u32 v93, v109, 16, 1
	v_lshrrev_b32_e32 v67, 16, v67
	v_add3_u32 v93, v109, v93, s41
	v_and_or_b32 v96, v93, s42, v67
	v_bfe_u32 v67, v111, 16, 1
	v_add3_u32 v67, v111, v67, s41
	v_bfe_u32 v93, v113, 16, 1
	v_lshrrev_b32_e32 v67, 16, v67
	v_add3_u32 v93, v113, v93, s41
	v_and_or_b32 v97, v93, s42, v67
	v_bitop3_b32 v93, s10, v78, v72 bitop3:0xc8
	v_or_b32_e32 v67, s10, v72
	v_or_b32_e32 v93, s11, v93
	v_cndmask_b32_e32 v67, v93, v67, vcc
	v_add_u32_e32 v67, s34, v67
	v_mad_u64_u32 v[98:99], s[22:23], v67, s33, 0
	v_ashrrev_i32_e32 v93, 31, v67
	v_mov_b32_e32 v100, v99
	v_mad_u64_u32 v[100:101], s[22:23], v93, s33, v[100:101]
	v_mov_b32_e32 v99, v100
	v_lshl_add_u64 v[98:99], v[98:99], 1, s[6:7]
	v_lshl_add_u64 v[98:99], v[98:99], 0, s[2:3]
	v_lshl_add_u64 v[98:99], v[98:99], 0, v[68:69]
	global_store_dwordx4 v[98:99], v[94:97], off nt
	s_waitcnt lgkmcnt(0)
	s_cselect_b64 s[22:23], -1, 0
	s_and_b64 vcc, exec, s[22:23]
	s_cbranch_vccnz .LBB0_2003
	s_mul_hi_i32 s2, s44, 0x2aaaaaab
	s_lshr_b32 s3, s2, 31
	s_ashr_i32 s2, s2, 9
	s_add_i32 s24, s2, s3
	s_mul_i32 s2, s24, 0xfffff400
	s_ashr_i32 s25, s24, 31
	s_add_i32 s19, s44, s2
	s_lshl_b64 s[2:3], s[24:25], 21
	s_add_u32 s8, s2, 0x2000000
	s_addc_u32 s9, s3, 0
	s_lshl_b32 s45, s24, 11
	s_cmpk_gt_i32 s19, 0x3ff
	s_mov_b64 s[10:11], -1
	s_cbranch_scc0 .LBB0_2000
	s_mul_i32 s2, s24, 0xc00
	s_sub_i32 s10, s44, s2
	s_cmpk_gt_u32 s19, 0x7ff
	s_mov_b64 s[6:7], -1
	s_cbranch_scc0 .LBB0_1998
	s_add_i32 s21, s10, 0xfffff800
	s_lshl_b64 s[2:3], s[8:9], 2
	s_add_u32 s2, s31, s2
	s_addc_u32 s3, s30, s3
	s_mov_b64 s[6:7], 0

; #define LAS __attribute__((address_space(3)))
; __device__ __forceinline__ unsigned pk2(float lo, float hi) { return f2bf(lo) | (f2bf(hi) << 16); }
;     __device__ __forceinline__ const float* x() const { return (const float*)ld(0); }
;     __device__ __forceinline__ const float* c() const { return (const float*)ld(1); }
; template <bool NT = true> __device__ __forceinline__ void cvt_store(const CvtItem& d, const f32x4 (&v)[8], LAS float* scr, int lane) {
;     const int rr = lane >> 3, c4 = (lane & 7) * 4;
; #pragma unroll
;     for (int q = 0; q < 8; ++q) { LAS float* t = scr + (8 * q + rr) * 33 + c4; t[0] = v[q].x; t[1] = v[q].y; t[2] = v[q].z; t[3] = v[q].w; }
;     asm volatile("s_waitcnt lgkmcnt(0)" ::: "memory");
;     const int c = lane & 7;
; #pragma unroll
;     for (int j = 0; j < 4; ++j) { const int n = (lane >> 3) + 8 * j; const LAS float* s = scr + (8 * c) * 33 + n;
;         u32x4 o; o.x = pk2(s[0 * 33], s[1 * 33]); o.y = pk2(s[2 * 33], s[3 * 33]); o.z = pk2(s[4 * 33], s[5 * 33]); o.w = pk2(s[6 * 33], s[7 * 33]);
;         const int ng = d.n0 + n, drow = d.row_off + (d.ilv ? ((ng >> 7) * 256 + (ng & 127)) : ng);
;         if (NT) __builtin_nontemporal_store(o, (u32x4*)(d.dst + (size_t)drow * d.K + d.k0 + 8 * c)); else *(u32x4*)(d.dst + (size_t)drow * d.K + d.k0 + 8 * c) = o; }
;     asm volatile("s_waitcnt lgkmcnt(0)" ::: "memory");
; }
; __device__ __forceinline__ void convert_moe_items(const Ctx& a, int layer, LAS unsigned char* lds, int it0, int it1, int widx, int nw, int wave, int lane) {
;     ...
;         cvt_store(db, vb, scr, lane);
;         hb = (it + nw < it1);
;         if (hb) { db = decode(it + nw); cvt_load(db, vb, lane); }
.Lcvt_p15_m:
	s_waitcnt vmcnt(12)
	ds_write2_b32 v74, v34, v35 offset1:1
	ds_write2_b32 v74, v36, v37 offset0:2 offset1:3
	ds_write2_b32 v79, v38, v39 offset1:1
	ds_write2_b32 v80, v40, v41 offset1:1
	ds_write2_b32 v81, v42, v43 offset1:1
	ds_write2_b32 v82, v44, v45 offset1:1
	ds_write2_b32 v83, v46, v47 offset1:1
	ds_write2_b32 v84, v48, v49 offset1:1
	ds_write2_b32 v85, v50, v51 offset1:1
	ds_write2_b32 v86, v52, v53 offset1:1
	ds_write2_b32 v87, v54, v55 offset1:1
	ds_write2_b32 v88, v56, v57 offset1:1
	ds_write2_b32 v89, v58, v59 offset1:1
	ds_write2_b32 v90, v60, v61 offset1:1
	ds_write2_b32 v91, v62, v63 offset1:1
	ds_write2_b32 v92, v64, v65 offset1:1
	s_waitcnt lgkmcnt(0)
	ds_read2_b32 v[84:85], v73 offset1:8
	ds_read2_b32 v[86:87], v73 offset0:33 offset1:41
	ds_read2_b32 v[88:89], v73 offset0:66 offset1:74
	ds_read2_b32 v[90:91], v73 offset0:99 offset1:107
	ds_read2_b32 v[92:93], v73 offset0:132 offset1:140
	s_waitcnt lgkmcnt(4)
	v_bfe_u32 v67, v84, 16, 1
	v_add3_u32 v67, v84, v67, s41
	s_waitcnt lgkmcnt(3)
	v_bfe_u32 v79, v86, 16, 1
	v_lshrrev_b32_e32 v67, 16, v67
	v_add3_u32 v79, v86, v79, s41
	ds_read2_b32 v[94:95], v73 offset0:165 offset1:173
	v_and_or_b32 v80, v79, s42, v67
	s_waitcnt lgkmcnt(3)
	v_bfe_u32 v67, v88, 16, 1
	v_add3_u32 v67, v88, v67, s41
	s_waitcnt lgkmcnt(2)
	v_bfe_u32 v79, v90, 16, 1
	ds_read2_b32 v[96:97], v73 offset0:198 offset1:206
	v_lshrrev_b32_e32 v67, 16, v67
	v_add3_u32 v79, v90, v79, s41
	ds_read2_b32 v[98:99], v73 offset0:231 offset1:239
	v_and_or_b32 v81, v79, s42, v67
	s_waitcnt lgkmcnt(3)
	v_bfe_u32 v67, v92, 16, 1
	v_add3_u32 v67, v92, v67, s41
	s_waitcnt lgkmcnt(2)
	v_bfe_u32 v79, v94, 16, 1
	v_lshrrev_b32_e32 v67, 16, v67
	v_add3_u32 v79, v94, v79, s41
	v_and_or_b32 v82, v79, s42, v67
	s_waitcnt lgkmcnt(1)
	v_bfe_u32 v67, v96, 16, 1
	v_add3_u32 v67, v96, v67, s41
	s_waitcnt lgkmcnt(0)
	v_bfe_u32 v79, v98, 16, 1
	v_lshrrev_b32_e32 v67, 16, v67
	v_add3_u32 v79, v98, v79, s41
	v_and_or_b32 v83, v79, s42, v67
	v_add_u32_e32 v67, s20, v1
	s_cmp_eq_u32 s36, 0
	v_lshlrev_b32_e32 v79, 1, v67
	v_and_b32_e32 v84, 0x7f, v67
	v_and_or_b32 v79, v79, s43, v84
	s_cselect_b64 vcc, -1, 0
	v_cndmask_b32_e32 v67, v79, v67, vcc
	v_add_u32_e32 v67, s38, v67
	v_mad_u64_u32 v[100:101], s[2:3], v67, s37, 0
	v_ashrrev_i32_e32 v79, 31, v67
	v_mov_b32_e32 v84, v101
	v_mad_u64_u32 v[102:103], s[2:3], v79, s37, v[84:85]
	v_mov_b32_e32 v101, v102
	s_ashr_i32 s19, s18, 31
	v_lshl_add_u64 v[100:101], v[100:101], 1, s[12:13]
	s_lshl_b64 s[2:3], s[18:19], 1
	v_bfe_u32 v67, v85, 16, 1
	v_lshl_add_u64 v[100:101], v[100:101], 0, s[2:3]
	v_add3_u32 v67, v85, v67, s41
	v_bfe_u32 v79, v87, 16, 1
	v_lshl_add_u64 v[100:101], v[100:101], 0, v[68:69]
	v_lshrrev_b32_e32 v67, 16, v67
	v_add3_u32 v79, v87, v79, s41
	global_store_dwordx4 v[100:101], v[80:83], off nt
	s_nop 1
	v_and_or_b32 v80, v79, s42, v67
	v_bfe_u32 v67, v89, 16, 1
	v_add3_u32 v67, v89, v67, s41
	v_bfe_u32 v79, v91, 16, 1
	v_lshrrev_b32_e32 v67, 16, v67
	v_add3_u32 v79, v91, v79, s41
	v_and_or_b32 v81, v79, s42, v67
	v_bfe_u32 v67, v93, 16, 1
	v_add3_u32 v67, v93, v67, s41
	v_bfe_u32 v79, v95, 16, 1
	v_lshrrev_b32_e32 v67, 16, v67
	v_add3_u32 v79, v95, v79, s41
	v_and_or_b32 v82, v79, s42, v67
	v_bfe_u32 v67, v97, 16, 1
	v_add3_u32 v67, v97, v67, s41
	v_bfe_u32 v79, v99, 16, 1
	v_lshrrev_b32_e32 v67, 16, v67
	v_add3_u32 v79, v99, v79, s41
	v_and_or_b32 v83, v79, s42, v67
	v_add_u32_e32 v67, s20, v70
	v_lshlrev_b32_e32 v79, 1, v67
	v_and_b32_e32 v84, 0x7f, v67
	v_and_or_b32 v79, v79, s43, v84
	v_cndmask_b32_e32 v67, v79, v67, vcc
	v_add_u32_e32 v67, s38, v67
	v_mad_u64_u32 v[84:85], s[14:15], v67, s37, 0
	v_ashrrev_i32_e32 v79, 31, v67
	v_mov_b32_e32 v86, v85
	v_mad_u64_u32 v[86:87], s[14:15], v79, s37, v[86:87]
	v_mov_b32_e32 v85, v86
	v_lshl_add_u64 v[84:85], v[84:85], 1, s[12:13]
	v_lshl_add_u64 v[84:85], v[84:85], 0, s[2:3]
	ds_read2_b32 v[86:87], v73 offset0:16 offset1:24
	v_lshl_add_u64 v[84:85], v[84:85], 0, v[68:69]
	global_store_dwordx4 v[84:85], v[80:83], off nt
	ds_read2_b32 v[84:85], v73 offset0:49 offset1:57
	ds_read2_b32 v[88:89], v73 offset0:82 offset1:90
	ds_read2_b32 v[90:91], v73 offset0:115 offset1:123
	s_waitcnt lgkmcnt(3)
; #define LAS __attribute__((address_space(3)))
; __device__ __forceinline__ unsigned pk2(float lo, float hi) { return f2bf(lo) | (f2bf(hi) << 16); }
;     __device__ __forceinline__ const float* x() const { return (const float*)ld(0); }
;     __device__ __forceinline__ const float* c() const { return (const float*)ld(1); }
; template <bool NT = true> __device__ __forceinline__ void cvt_store(const CvtItem& d, const f32x4 (&v)[8], LAS float* scr, int lane) {
;     ...
;     for (int j = 0; j < 4; ++j) { const int n = (lane >> 3) + 8 * j; const LAS float* s = scr + (8 * c) * 33 + n;
;         u32x4 o; o.x = pk2(s[0 * 33], s[1 * 33]); o.y = pk2(s[2 * 33], s[3 * 33]); o.z = pk2(s[4 * 33], s[5 * 33]); o.w = pk2(s[6 * 33], s[7 * 33]);
;         const int ng = d.n0 + n, drow = d.row_off + (d.ilv ? ((ng >> 7) * 256 + (ng & 127)) : ng);
;         if (NT) __builtin_nontemporal_store(o, (u32x4*)(d.dst + (size_t)drow * d.K + d.k0 + 8 * c)); else *(u32x4*)(d.dst + (size_t)drow * d.K + d.k0 + 8 * c) = o; }
;     asm volatile("s_waitcnt lgkmcnt(0)" ::: "memory");
; __device__ __forceinline__ void convert_moe_items(const Ctx& a, int layer, LAS unsigned char* lds, int it0, int it1, int widx, int nw, int wave, int lane) {
;     ...
;     auto decode = [&](int it) { CvtItem d; const int e = it / PER_E; int r = it % PER_E; const size_t eo = ((size_t)layer * NE + e) * (size_t)DM * FE;
;         if (r < I_G)          { d.src = wg + eo; d.dst = WGU; d.N = FE; d.K = DM; d.row_off = e * 2048; d.ilv = 1; }
;         else if (r < 2 * I_G) { r -= I_G; d.src = wu + eo; d.dst = WGU; d.N = FE; d.K = DM; d.row_off = e * 2048 + 128; d.ilv = 1; }
;         else                  { r -= 2 * I_G; d.src = wd + eo; d.dst = WD; d.N = DM; d.K = FE; d.row_off = e * 2048; d.ilv = 0; }
;         const int nblk = d.N / 32; d.k0 = 64 * (r / nblk); d.n0 = 32 * (r % nblk); return d; };
;     ...
;         hb = (it + nw < it1);
;         if (hb) { db = decode(it + nw); cvt_load(db, vb, lane); }
;         if (!ha) break;
;     }
	v_bfe_u32 v67, v86, 16, 1
	v_add3_u32 v67, v86, v67, s41
	s_waitcnt lgkmcnt(2)
	v_bfe_u32 v79, v84, 16, 1
	ds_read2_b32 v[92:93], v73 offset0:148 offset1:156
	v_lshrrev_b32_e32 v67, 16, v67
	v_add3_u32 v79, v84, v79, s41
	ds_read2_b32 v[94:95], v73 offset0:181 offset1:189
	v_and_or_b32 v80, v79, s42, v67
	s_waitcnt lgkmcnt(3)
	v_bfe_u32 v67, v88, 16, 1
	v_add3_u32 v67, v88, v67, s41
	s_waitcnt lgkmcnt(2)
	v_bfe_u32 v79, v90, 16, 1
	ds_read2_b32 v[96:97], v73 offset0:214 offset1:222
	v_lshrrev_b32_e32 v67, 16, v67
	v_add3_u32 v79, v90, v79, s41
	ds_read2_b32 v[98:99], v73 offset0:247 offset1:255
	v_and_or_b32 v81, v79, s42, v67
	s_waitcnt lgkmcnt(3)
	v_bfe_u32 v67, v92, 16, 1
	v_add3_u32 v67, v92, v67, s41
	s_waitcnt lgkmcnt(2)
	v_bfe_u32 v79, v94, 16, 1
	v_lshrrev_b32_e32 v67, 16, v67
	v_add3_u32 v79, v94, v79, s41
	v_and_or_b32 v82, v79, s42, v67
	s_waitcnt lgkmcnt(1)
	v_bfe_u32 v67, v96, 16, 1
	v_add3_u32 v67, v96, v67, s41
	s_waitcnt lgkmcnt(0)
	v_bfe_u32 v79, v98, 16, 1
	v_lshrrev_b32_e32 v67, 16, v67
	v_add3_u32 v79, v98, v79, s41
	v_and_or_b32 v83, v79, s42, v67
	v_add_u32_e32 v67, s20, v71
	v_lshlrev_b32_e32 v79, 1, v67
	v_and_b32_e32 v84, 0x7f, v67
	v_and_or_b32 v79, v79, s43, v84
	v_cndmask_b32_e32 v67, v79, v67, vcc
	v_add_u32_e32 v67, s38, v67
	v_mad_u64_u32 v[100:101], s[14:15], v67, s37, 0
	v_ashrrev_i32_e32 v79, 31, v67
	v_mov_b32_e32 v84, v101
	v_mad_u64_u32 v[102:103], s[14:15], v79, s37, v[84:85]
	v_mov_b32_e32 v101, v102
	v_lshl_add_u64 v[100:101], v[100:101], 1, s[12:13]
	v_bfe_u32 v67, v87, 16, 1
	v_lshl_add_u64 v[100:101], v[100:101], 0, s[2:3]
	v_add3_u32 v67, v87, v67, s41
	v_bfe_u32 v79, v85, 16, 1
	v_lshl_add_u64 v[100:101], v[100:101], 0, v[68:69]
	v_lshrrev_b32_e32 v67, 16, v67
	v_add3_u32 v79, v85, v79, s41
	global_store_dwordx4 v[100:101], v[80:83], off nt
	s_nop 1
	v_and_or_b32 v80, v79, s42, v67
	v_bfe_u32 v67, v89, 16, 1
	v_add3_u32 v67, v89, v67, s41
	v_bfe_u32 v79, v91, 16, 1
	v_lshrrev_b32_e32 v67, 16, v67
	v_add3_u32 v79, v91, v79, s41
	v_and_or_b32 v81, v79, s42, v67
	v_bfe_u32 v67, v93, 16, 1
	v_add3_u32 v67, v93, v67, s41
	v_bfe_u32 v79, v95, 16, 1
	v_lshrrev_b32_e32 v67, 16, v67
	v_add3_u32 v79, v95, v79, s41
	v_and_or_b32 v82, v79, s42, v67
	v_bfe_u32 v67, v97, 16, 1
	v_add3_u32 v67, v97, v67, s41
	v_bfe_u32 v79, v99, 16, 1
	v_lshrrev_b32_e32 v67, 16, v67
	v_add3_u32 v79, v99, v79, s41
	v_and_or_b32 v83, v79, s42, v67
	v_add_u32_e32 v67, s20, v72
	v_lshlrev_b32_e32 v79, 1, v67
	v_and_b32_e32 v84, 0x7f, v67
	v_and_or_b32 v79, v79, s43, v84
	v_cndmask_b32_e32 v67, v79, v67, vcc
	v_add_u32_e32 v67, s38, v67
	v_mad_u64_u32 v[84:85], s[14:15], v67, s37, 0
	v_ashrrev_i32_e32 v79, 31, v67
	v_mov_b32_e32 v86, v85
	v_mad_u64_u32 v[86:87], s[14:15], v79, s37, v[86:87]
	v_mov_b32_e32 v85, v86
	v_lshl_add_u64 v[84:85], v[84:85], 1, s[12:13]
	v_lshl_add_u64 v[84:85], v[84:85], 0, s[2:3]
	v_lshl_add_u64 v[84:85], v[84:85], 0, v[68:69]
	global_store_dwordx4 v[84:85], v[80:83], off nt
	s_add_i32 s2, s40, s35
	s_waitcnt lgkmcnt(0)
	s_cmp_lt_i32 s2, 0xc000
	s_cselect_b64 s[14:15], -1, 0
	s_cmp_gt_i32 s2, 0xbfff
	s_cbranch_scc1 .LBB0_1992
	s_mul_hi_i32 s3, s2, 0x2aaaaaab
	s_lshr_b32 s9, s3, 31
	s_ashr_i32 s3, s3, 9
	s_add_i32 s12, s3, s9
	s_mul_i32 s3, s12, 0xc00
	s_ashr_i32 s13, s12, 31
	s_sub_i32 s11, s2, s3
	s_lshl_b64 s[2:3], s[12:13], 21
	s_add_u32 s18, s2, 0x2000000
	s_addc_u32 s19, s3, 0
	s_lshl_b32 s24, s12, 11
	s_cmpk_gt_i32 s11, 0x3ff
	s_mov_b64 s[20:21], -1
	s_cbranch_scc0 .LBB0_2010
	s_cmpk_gt_u32 s11, 0x7ff
	s_mov_b64 s[12:13], -1
	s_cbranch_scc0 .LBB0_2008
	s_add_i32 s9, s11, 0xfffff800
	s_lshl_b64 s[2:3], s[18:19], 2
	s_add_u32 s2, s31, s2
	s_addc_u32 s3, s30, s3
	s_mov_b64 s[12:13], 0
